# v66 + gate/up epilogues (both call sites) skip the store of 32-row groups that are entirely padding rows
# baseline (speedup 1.0000x reference)
.LBB0_801:
	v_and_b32_e32 v5, 15, v4
	s_add_i32 s0, 0, 0x21000
	v_or_b32_e32 v6, s53, v5
	v_lshl_add_u32 v253, v4, 4, s0
	v_and_b32_e32 v7, 48, v4
	v_lshlrev_b32_e32 v8, 6, v6
	s_movk_i32 s0, 0x3c0
	v_and_or_b32 v8, v8, s0, v7
	v_lshlrev_b32_e32 v4, 2, v4
	s_add_u32 s0, s18, 0x80
	v_lshl_or_b32 v5, v5, 6, v7
	v_and_b32_e32 v4, 32, v4
	s_addc_u32 s1, s19, 0
	v_bitop3_b32 v158, v5, s56, v4 bitop3:0xde
	s_waitcnt vmcnt(2)
	s_barrier
	s_add_i32 m0, s7, 0x18000
	v_lshl_add_u64 v[4:5], s[0:1], 0, v[140:141]
	global_load_lds_dwordx4 v[4:5], off
	s_add_i32 m0, s7, 0x1a000
	v_lshl_add_u64 v[4:5], s[0:1], 0, v[142:143]
	s_add_u32 s0, s90, 0x12800080
	s_addc_u32 s1, s91, 0
	s_add_i32 s60, s7, 0x8000
	global_load_lds_dwordx4 v[4:5], off
	s_mov_b32 m0, s60
	v_lshl_add_u64 v[4:5], s[0:1], 0, v[0:1]
	s_add_i32 s61, s7, 0xa000
	global_load_lds_dwordx4 v[4:5], off
	v_lshl_add_u64 v[4:5], s[0:1], 0, v[144:145]
	s_add_u32 s0, s18, 0x40080
	s_mov_b32 m0, s61
	s_addc_u32 s1, s19, 0
	global_load_lds_dwordx4 v[4:5], off
	s_add_i32 m0, s7, 0x1c000
	v_lshl_add_u64 v[4:5], s[0:1], 0, v[140:141]
	global_load_lds_dwordx4 v[4:5], off
	v_lshl_add_u64 v[4:5], s[0:1], 0, v[142:143]
	s_add_i32 m0, s7, 0x1e000
	v_lshlrev_b32_e32 v6, 2, v6
	global_load_lds_dwordx4 v[4:5], off
	v_and_b32_e32 v6, 32, v6
	s_waitcnt vmcnt(6)
	v_readlane_b32 s0, v255, 25
	v_bitop3_b32 v6, v8, s55, v6 bitop3:0xde
	s_cmpk_lt_u32 s0, 0x100
	s_cselect_b64 s[22:23], -1, 0
	s_add_i32 s62, 0, 0x10000
	s_add_i32 s63, 0, 0x14000
	v_add_u32_e32 v143, 0, v6
	v_mov_b32_e32 v145, 0x7f7f7f7f
	s_mov_b32 s24, 0x3c800000
	s_mov_b32 s64, 0xc0c00000
	v_mov_b32_e32 v159, 0x41000000
	v_mov_b32_e32 v4, v141
	v_mov_b32_e32 v5, v141
	v_mov_b32_e32 v6, v141
	v_mov_b32_e32 v7, v141
	v_mov_b32_e32 v8, v141
	v_mov_b32_e32 v9, v141
	v_mov_b32_e32 v10, v141
	v_mov_b32_e32 v11, v141
	v_mov_b32_e32 v12, v141
	v_mov_b32_e32 v13, v141
	v_mov_b32_e32 v14, v141
	v_mov_b32_e32 v15, v141
	v_mov_b32_e32 v16, v141
	v_mov_b32_e32 v17, v141
	v_mov_b32_e32 v18, v141
	v_mov_b32_e32 v19, v141
	v_mov_b32_e32 v20, v141
	v_mov_b32_e32 v21, v141
	v_mov_b32_e32 v22, v141
	v_mov_b32_e32 v23, v141
	v_mov_b32_e32 v24, v141
	v_mov_b32_e32 v25, v141
	v_mov_b32_e32 v26, v141
	v_mov_b32_e32 v27, v141
	v_mov_b32_e32 v232, v141
	v_mov_b32_e32 v233, v141
	v_mov_b32_e32 v234, v141
	v_mov_b32_e32 v235, v141
	v_mov_b32_e32 v32, v141
	v_mov_b32_e32 v33, v141
	v_mov_b32_e32 v34, v141
	v_mov_b32_e32 v35, v141
	v_mov_b32_e32 v36, v141
	v_mov_b32_e32 v37, v141
	v_mov_b32_e32 v38, v141
	v_mov_b32_e32 v39, v141
	v_mov_b32_e32 v40, v141
	v_mov_b32_e32 v41, v141
	v_mov_b32_e32 v42, v141
	v_mov_b32_e32 v43, v141
	v_mov_b32_e32 v44, v141
	v_mov_b32_e32 v45, v141
	v_mov_b32_e32 v46, v141
	v_mov_b32_e32 v47, v141
	v_mov_b32_e32 v48, v141
	v_mov_b32_e32 v49, v141
	v_mov_b32_e32 v50, v141
	v_mov_b32_e32 v51, v141
	v_mov_b32_e32 v52, v141
	v_mov_b32_e32 v53, v141
	v_mov_b32_e32 v54, v141
	v_mov_b32_e32 v55, v141
	v_mov_b32_e32 v56, v141
	v_mov_b32_e32 v57, v141
	v_mov_b32_e32 v58, v141
	v_mov_b32_e32 v59, v141
	v_mov_b32_e32 v60, v141
	v_mov_b32_e32 v61, v141
	v_mov_b32_e32 v62, v141
	v_mov_b32_e32 v63, v141
	v_mov_b32_e32 v64, v141
	v_mov_b32_e32 v65, v141
	v_mov_b32_e32 v66, v141
	v_mov_b32_e32 v67, v141
	v_mov_b32_e32 v28, v141
	v_mov_b32_e32 v29, v141
	v_mov_b32_e32 v30, v141
	v_mov_b32_e32 v31, v141
	v_mov_b32_e32 v72, v141
	v_mov_b32_e32 v73, v141
	v_mov_b32_e32 v74, v141
	v_mov_b32_e32 v75, v141
	v_mov_b32_e32 v76, v141
	v_mov_b32_e32 v77, v141
	v_mov_b32_e32 v78, v141
	v_mov_b32_e32 v79, v141
	v_mov_b32_e32 v80, v141
	v_mov_b32_e32 v81, v141
	v_mov_b32_e32 v82, v141
	v_mov_b32_e32 v83, v141
	v_mov_b32_e32 v84, v141
	v_mov_b32_e32 v85, v141
	v_mov_b32_e32 v86, v141
	v_mov_b32_e32 v87, v141
	v_mov_b32_e32 v88, v141
	v_mov_b32_e32 v89, v141
	v_mov_b32_e32 v90, v141
	v_mov_b32_e32 v91, v141
	v_mov_b32_e32 v92, v141
	v_mov_b32_e32 v93, v141
	v_mov_b32_e32 v94, v141
	v_mov_b32_e32 v95, v141
	v_mov_b32_e32 v96, v141
	v_mov_b32_e32 v97, v141
	v_mov_b32_e32 v98, v141
	v_mov_b32_e32 v99, v141
	v_mov_b32_e32 v100, v141
	v_mov_b32_e32 v101, v141
	v_mov_b32_e32 v102, v141
	v_mov_b32_e32 v103, v141
	v_mov_b32_e32 v104, v141
	v_mov_b32_e32 v105, v141
	v_mov_b32_e32 v106, v141
	v_mov_b32_e32 v107, v141
	v_mov_b32_e32 v108, v141
	v_mov_b32_e32 v109, v141
	v_mov_b32_e32 v110, v141
	v_mov_b32_e32 v111, v141
	v_mov_b32_e32 v112, v141
	v_mov_b32_e32 v113, v141
	v_mov_b32_e32 v114, v141
	v_mov_b32_e32 v115, v141
	v_mov_b32_e32 v116, v141
	v_mov_b32_e32 v117, v141
	v_mov_b32_e32 v118, v141
	v_mov_b32_e32 v119, v141
	v_mov_b32_e32 v120, v141
	v_mov_b32_e32 v121, v141
	v_mov_b32_e32 v122, v141
	v_mov_b32_e32 v123, v141
	v_mov_b32_e32 v124, v141
	v_mov_b32_e32 v125, v141
	v_mov_b32_e32 v126, v141
	v_mov_b32_e32 v127, v141
	v_mov_b32_e32 v128, v141
	v_mov_b32_e32 v129, v141
	v_mov_b32_e32 v130, v141
	v_mov_b32_e32 v131, v141
	s_barrier
	s_mov_b32 s97, 0x7fffffff
	s_branch .LBB0_804
.LBB0_802:
	s_mov_b32 s97, s67
	v_mov_b32_e32 v4, 0
	s_waitcnt lgkmcnt(0)
	v_mov_b32_e32 v144, v1
	s_mov_b32 s2, s65
	s_mov_b32 s6, s28
	s_mov_b32 s4, s26
	s_mov_b64 s[18:19], s[0:1]
	s_mov_b32 s59, s68
	v_mov_b32_e32 v5, v4
	v_mov_b32_e32 v6, v4
	v_mov_b32_e32 v7, v4
	v_mov_b32_e32 v8, v4
	v_mov_b32_e32 v9, v4
	v_mov_b32_e32 v10, v4
	v_mov_b32_e32 v11, v4
	v_mov_b32_e32 v12, v4
	v_mov_b32_e32 v13, v4
	v_mov_b32_e32 v14, v4
	v_mov_b32_e32 v15, v4
	v_mov_b32_e32 v16, v4
	v_mov_b32_e32 v17, v4
	v_mov_b32_e32 v18, v4
	v_mov_b32_e32 v19, v4
	v_mov_b32_e32 v20, v4
	v_mov_b32_e32 v21, v4
	v_mov_b32_e32 v22, v4
	v_mov_b32_e32 v23, v4
	v_mov_b32_e32 v24, v4
	v_mov_b32_e32 v25, v4
	v_mov_b32_e32 v26, v4
	v_mov_b32_e32 v27, v4
	v_mov_b32_e32 v232, v4
	v_mov_b32_e32 v233, v4
	v_mov_b32_e32 v234, v4
	v_mov_b32_e32 v235, v4
	v_mov_b32_e32 v32, v4
	v_mov_b32_e32 v33, v4
	v_mov_b32_e32 v34, v4
	v_mov_b32_e32 v35, v4
	v_mov_b32_e32 v36, v4
	v_mov_b32_e32 v37, v4
	v_mov_b32_e32 v38, v4
	v_mov_b32_e32 v39, v4
	v_mov_b32_e32 v40, v4
	v_mov_b32_e32 v41, v4
	v_mov_b32_e32 v42, v4
	v_mov_b32_e32 v43, v4
	v_mov_b32_e32 v44, v4
	v_mov_b32_e32 v45, v4
	v_mov_b32_e32 v46, v4
	v_mov_b32_e32 v47, v4
	v_mov_b32_e32 v48, v4
	v_mov_b32_e32 v49, v4
	v_mov_b32_e32 v50, v4
	v_mov_b32_e32 v51, v4
	v_mov_b32_e32 v52, v4
	v_mov_b32_e32 v53, v4
	v_mov_b32_e32 v54, v4
	v_mov_b32_e32 v55, v4
	v_mov_b32_e32 v56, v4
	v_mov_b32_e32 v57, v4
	v_mov_b32_e32 v58, v4
	v_mov_b32_e32 v59, v4
	v_mov_b32_e32 v60, v4
	v_mov_b32_e32 v61, v4
	v_mov_b32_e32 v62, v4
	v_mov_b32_e32 v63, v4
	v_mov_b32_e32 v64, v4
	v_mov_b32_e32 v65, v4
	v_mov_b32_e32 v66, v4
	v_mov_b32_e32 v67, v4
	v_mov_b32_e32 v28, v4
	v_mov_b32_e32 v29, v4
	v_mov_b32_e32 v30, v4
	v_mov_b32_e32 v31, v4
	v_mov_b32_e32 v72, v4
	v_mov_b32_e32 v73, v4
	v_mov_b32_e32 v74, v4
	v_mov_b32_e32 v75, v4
	v_mov_b32_e32 v76, v4
	v_mov_b32_e32 v77, v4
	v_mov_b32_e32 v78, v4
	v_mov_b32_e32 v79, v4
	v_mov_b32_e32 v80, v4
	v_mov_b32_e32 v81, v4
	v_mov_b32_e32 v82, v4
	v_mov_b32_e32 v83, v4
	v_mov_b32_e32 v84, v4
	v_mov_b32_e32 v85, v4
	v_mov_b32_e32 v86, v4
	v_mov_b32_e32 v87, v4
	v_mov_b32_e32 v88, v4
	v_mov_b32_e32 v89, v4
	v_mov_b32_e32 v90, v4
	v_mov_b32_e32 v91, v4
	v_mov_b32_e32 v92, v4
	v_mov_b32_e32 v93, v4
	v_mov_b32_e32 v94, v4
	v_mov_b32_e32 v95, v4
	v_mov_b32_e32 v96, v4
	v_mov_b32_e32 v97, v4
	v_mov_b32_e32 v98, v4
	v_mov_b32_e32 v99, v4
	v_mov_b32_e32 v100, v4
	v_mov_b32_e32 v101, v4
	v_mov_b32_e32 v102, v4
	v_mov_b32_e32 v103, v4
	v_mov_b32_e32 v104, v4
	v_mov_b32_e32 v105, v4
	v_mov_b32_e32 v106, v4
	v_mov_b32_e32 v107, v4
	v_mov_b32_e32 v108, v4
	v_mov_b32_e32 v109, v4
	v_mov_b32_e32 v110, v4
	v_mov_b32_e32 v111, v4
	v_mov_b32_e32 v112, v4
	v_mov_b32_e32 v113, v4
	v_mov_b32_e32 v114, v4
	v_mov_b32_e32 v115, v4
	v_mov_b32_e32 v116, v4
	v_mov_b32_e32 v117, v4
	v_mov_b32_e32 v118, v4
	v_mov_b32_e32 v119, v4
	v_mov_b32_e32 v120, v4
	v_mov_b32_e32 v121, v4
	v_mov_b32_e32 v122, v4
	v_mov_b32_e32 v123, v4
	v_mov_b32_e32 v124, v4
	v_mov_b32_e32 v125, v4
	v_mov_b32_e32 v126, v4
	v_mov_b32_e32 v127, v4
	v_mov_b32_e32 v128, v4
	v_mov_b32_e32 v129, v4
	v_mov_b32_e32 v130, v4
	v_mov_b32_e32 v131, v4

.LBB0_837:
	s_sub_i32 s96, s97, s53
	s_lshl_b32 s5, s6, 7
	v_mbcnt_lo_u32_b32 v1, -1, 0
	v_mbcnt_hi_u32_b32 v1, -1, v1
	s_or_b32 s5, s5, s54
	v_ashrrev_i32_e32 v141, 4, v1
	v_lshl_add_u32 v146, v141, 3, s5
	s_ashr_i32 s5, s4, 31
	v_readlane_b32 s72, v255, 31
	s_lshl_b64 s[38:39], s[4:5], 13
	v_readlane_b32 s76, v255, 35
	v_readlane_b32 s77, v255, 36
	s_add_u32 s40, s76, s38
	v_readlane_b32 s80, v255, 39
	s_addc_u32 s41, s77, s39
	v_ashrrev_i32_e32 v147, 31, v146
	v_readlane_b32 s81, v255, 40
	v_lshlrev_b64 v[68:69], 2, v[146:147]
	s_add_u32 s38, s80, s38
	v_lshl_add_u64 v[70:71], s[40:41], 0, v[68:69]
	s_addc_u32 s39, s81, s39
	global_load_dwordx4 v[136:139], v[70:71], off
	global_load_dwordx4 v[132:135], v[70:71], off offset:16
	v_lshl_add_u64 v[148:149], s[38:39], 0, v[68:69]
	global_load_dwordx4 v[68:71], v[148:149], off
	global_load_dwordx4 v[160:163], v[148:149], off offset:16
	v_and_b32_e32 v141, 1, v141
	v_and_b32_e32 v1, 15, v1
	v_lshlrev_b32_e32 v150, 4, v141
	s_add_i32 s5, s2, s53
	v_add3_u32 v150, s5, v1, v150
	v_ashrrev_i32_e32 v151, 31, v150
	v_lshlrev_b32_e32 v141, 3, v141
	v_lshlrev_b64 v[150:151], 11, v[150:151]
	v_sub_co_u32_e32 v148, vcc, 0, v141
	v_lshl_add_u64 v[150:151], s[14:15], 0, v[150:151]
	v_lshl_add_u64 v[146:147], v[150:151], 0, v[146:147]
	v_subb_co_u32_e64 v149, s[38:39], 0, 0, vcc
	v_lshl_add_u64 v[146:147], v[146:147], 0, v[148:149]
	v_mov_b32_e32 v164, 0
	v_mov_b32_e32 v165, 0
	s_mov_b32 s5, 0x10000
	v_readlane_b32 s73, v255, 32
	v_readlane_b32 s74, v255, 33
	v_readlane_b32 s75, v255, 34
	v_readlane_b32 s78, v255, 37
	v_readlane_b32 s79, v255, 38
	v_readlane_b32 s82, v255, 41
	v_readlane_b32 s83, v255, 42
	v_readlane_b32 s84, v255, 43
	v_readlane_b32 s85, v255, 44
	v_readlane_b32 s86, v255, 45
	v_readlane_b32 s87, v255, 46
	s_waitcnt vmcnt(0)
	v_pk_fma_f32 v[166:167], v[128:129], s[24:25], v[136:137] op_sel_hi:[1,0,1]
	v_pk_fma_f32 v[156:157], v[130:131], s[24:25], v[138:139] op_sel_hi:[1,0,1]
	v_pk_add_f32 v[154:155], v[68:69], 1.0 op_sel_hi:[1,0]
	v_min_f32_e32 v68, 0x40e00000, v166
	v_min_f32_e32 v69, 0x40e00000, v167
	v_pk_fma_f32 v[168:169], v[126:127], s[24:25], v[134:135] op_sel_hi:[1,0,1]
	v_mul_f32_e32 v1, 0xc01d265f, v68
	v_mul_f32_e32 v141, 0xc01d265f, v69
	v_pk_add_f32 v[152:153], v[70:71], 1.0 op_sel_hi:[1,0]
	v_pk_add_f32 v[150:151], v[160:161], 1.0 op_sel_hi:[1,0]
	v_min_f32_e32 v70, 0x40e00000, v156
	v_min_f32_e32 v71, 0x40e00000, v157
	v_min_f32_e32 v160, 0x40e00000, v168
	v_min_f32_e32 v161, 0x40e00000, v169
	v_exp_f32_e32 v174, v1
	v_exp_f32_e32 v175, v141
	v_mul_f32_e32 v176, 0xc01d265f, v70
	v_mul_f32_e32 v177, 0xc01d265f, v71
	v_mul_f32_e32 v180, 0xc01d265f, v160
	v_mul_f32_e32 v181, 0xc01d265f, v161
	v_exp_f32_e32 v176, v176
	v_exp_f32_e32 v177, v177
	v_exp_f32_e32 v180, v180
	v_exp_f32_e32 v181, v181
	v_pk_add_f32 v[174:175], v[174:175], 1.0 op_sel_hi:[1,0]
	v_pk_fma_f32 v[170:171], v[124:125], s[24:25], v[132:133] op_sel_hi:[1,0,1]
	v_rcp_f32_e32 v174, v174
	v_rcp_f32_e32 v175, v175
	v_min_f32_e32 v156, 0x40e00000, v170
	v_min_f32_e32 v157, 0x40e00000, v171
	v_pk_add_f32 v[176:177], v[176:177], 1.0 op_sel_hi:[1,0]
	v_pk_add_f32 v[180:181], v[180:181], 1.0 op_sel_hi:[1,0]
	v_mul_f32_e32 v178, 0xc01d265f, v156
	v_mul_f32_e32 v179, 0xc01d265f, v157
	v_rcp_f32_e32 v176, v176
	v_rcp_f32_e32 v177, v177
	v_rcp_f32_e32 v180, v180
	v_rcp_f32_e32 v181, v181
	v_pk_fma_f32 v[166:167], v[96:97], s[24:25], v[154:155] op_sel_hi:[1,0,1]
	v_exp_f32_e32 v178, v178
	v_exp_f32_e32 v179, v179
	v_pk_add_f32 v[148:149], v[162:163], 1.0 op_sel_hi:[1,0]
	v_med3_f32 v166, v166, s64, v159
	v_med3_f32 v167, v167, s64, v159
	v_pk_mul_f32 v[68:69], v[68:69], v[174:175]
	v_pk_fma_f32 v[162:163], v[98:99], s[24:25], v[152:153] op_sel_hi:[1,0,1]
	v_pk_fma_f32 v[168:169], v[94:95], s[24:25], v[148:149] op_sel_hi:[1,0,1]
	v_pk_mul_f32 v[68:69], v[166:167], v[68:69]
	v_pk_fma_f32 v[172:173], v[122:123], s[24:25], v[138:139] op_sel_hi:[1,0,1]
	v_med3_f32 v162, v162, s64, v159
	v_med3_f32 v163, v163, s64, v159
	v_med3_f32 v168, v168, s64, v159
	v_med3_f32 v169, v169, s64, v159
	v_pk_mul_f32 v[70:71], v[70:71], v[176:177]
	v_pk_mul_f32 v[160:161], v[160:161], v[180:181]
	v_cvt_pk_fp8_f32 v164, v68, v69
	v_pk_add_f32 v[178:179], v[178:179], 1.0 op_sel_hi:[1,0]
	v_pk_mul_f32 v[68:69], v[162:163], v[70:71]
	v_pk_mul_f32 v[70:71], v[168:169], v[160:161]
	v_min_f32_e32 v160, 0x40e00000, v172
	v_rcp_f32_e32 v178, v178
	v_rcp_f32_e32 v179, v179
	v_min_f32_e32 v161, 0x40e00000, v173
	v_mul_f32_e32 v141, 0xc01d265f, v160
	v_exp_f32_e32 v166, v141
	v_mul_f32_e32 v141, 0xc01d265f, v161
	v_cvt_pk_fp8_f32 v164, v68, v69 op_sel:[0,0,1]
	v_pk_fma_f32 v[68:69], v[120:121], s[24:25], v[136:137] op_sel_hi:[1,0,1]
	v_exp_f32_e32 v167, v141
	v_pk_fma_f32 v[170:171], v[92:93], s[24:25], v[150:151] op_sel_hi:[1,0,1]
	v_min_f32_e32 v68, 0x40e00000, v68
	v_med3_f32 v170, v170, s64, v159
	v_med3_f32 v171, v171, s64, v159
	v_pk_mul_f32 v[156:157], v[156:157], v[178:179]
	v_min_f32_e32 v69, 0x40e00000, v69
	v_mul_f32_e32 v1, 0xc01d265f, v68
	v_pk_mul_f32 v[156:157], v[170:171], v[156:157]
	v_exp_f32_e32 v162, v1
	v_mul_f32_e32 v1, 0xc01d265f, v69
	v_cvt_pk_fp8_f32 v165, v156, v157
	v_exp_f32_e32 v163, v1
	v_pk_add_f32 v[166:167], v[166:167], 1.0 op_sel_hi:[1,0]
	v_pk_fma_f32 v[156:157], v[88:89], s[24:25], v[154:155] op_sel_hi:[1,0,1]
	v_rcp_f32_e32 v166, v166
	v_rcp_f32_e32 v167, v167
	v_cvt_pk_fp8_f32 v165, v70, v71 op_sel:[0,0,1]
	v_pk_fma_f32 v[70:71], v[90:91], s[24:25], v[152:153] op_sel_hi:[1,0,1]
	v_pk_add_f32 v[162:163], v[162:163], 1.0 op_sel_hi:[1,0]
	v_med3_f32 v70, v70, s64, v159
	v_rcp_f32_e32 v162, v162
	v_rcp_f32_e32 v163, v163
	v_med3_f32 v71, v71, s64, v159
	v_pk_mul_f32 v[160:161], v[160:161], v[166:167]
	v_med3_f32 v156, v156, s64, v159
	v_pk_mul_f32 v[70:71], v[70:71], v[160:161]
	v_pk_fma_f32 v[160:161], v[116:117], s[24:25], v[132:133] op_sel_hi:[1,0,1]
	v_med3_f32 v157, v157, s64, v159
	v_min_f32_e32 v160, 0x40e00000, v160
	v_min_f32_e32 v161, 0x40e00000, v161
	v_mul_f32_e32 v1, 0xc01d265f, v160
	v_pk_mul_f32 v[68:69], v[68:69], v[162:163]
	v_exp_f32_e32 v168, v1
	v_mul_f32_e32 v1, 0xc01d265f, v161
	v_pk_mul_f32 v[68:69], v[156:157], v[68:69]
	v_pk_fma_f32 v[156:157], v[118:119], s[24:25], v[134:135] op_sel_hi:[1,0,1]
	v_exp_f32_e32 v169, v1
	v_min_f32_e32 v156, 0x40e00000, v156
	v_min_f32_e32 v157, 0x40e00000, v157
	v_mul_f32_e32 v1, 0xc01d265f, v156
	v_exp_f32_e32 v170, v1
	v_mul_f32_e32 v1, 0xc01d265f, v157
	v_exp_f32_e32 v171, v1
	v_pk_add_f32 v[168:169], v[168:169], 1.0 op_sel_hi:[1,0]
	v_pk_fma_f32 v[166:167], v[84:85], s[24:25], v[150:151] op_sel_hi:[1,0,1]
	v_rcp_f32_e32 v168, v168
	v_rcp_f32_e32 v169, v169
	v_pk_add_f32 v[170:171], v[170:171], 1.0 op_sel_hi:[1,0]
	v_med3_f32 v166, v166, s64, v159
	v_med3_f32 v167, v167, s64, v159
	v_rcp_f32_e32 v170, v170
	v_rcp_f32_e32 v171, v171
	v_pk_mul_f32 v[160:161], v[160:161], v[168:169]
	v_pk_fma_f32 v[162:163], v[86:87], s[24:25], v[148:149] op_sel_hi:[1,0,1]
	v_pk_mul_f32 v[160:161], v[166:167], v[160:161]
	v_mov_b32_e32 v166, 0
	v_mov_b32_e32 v167, 0
	v_cvt_pk_fp8_f32 v166, v68, v69
	v_cvt_pk_fp8_f32 v167, v160, v161
	v_med3_f32 v162, v162, s64, v159
	v_med3_f32 v163, v163, s64, v159
	v_pk_mul_f32 v[68:69], v[156:157], v[170:171]
	v_cvt_pk_fp8_f32 v166, v70, v71 op_sel:[0,0,1]
	v_pk_mul_f32 v[68:69], v[162:163], v[68:69]
	v_pk_fma_f32 v[70:71], v[112:113], s[24:25], v[136:137] op_sel_hi:[1,0,1]
	v_cvt_pk_fp8_f32 v167, v68, v69 op_sel:[0,0,1]
	v_min_f32_e32 v70, 0x40e00000, v70
	v_pk_fma_f32 v[68:69], v[114:115], s[24:25], v[138:139] op_sel_hi:[1,0,1]
	v_min_f32_e32 v71, 0x40e00000, v71
	v_mul_f32_e32 v1, 0xc01d265f, v70
	v_min_f32_e32 v68, 0x40e00000, v68
	v_exp_f32_e32 v162, v1
	v_mul_f32_e32 v1, 0xc01d265f, v71
	v_permlane16_swap_b32_e32 v164, v166
	v_permlane16_swap_b32_e32 v165, v167
	v_min_f32_e32 v69, 0x40e00000, v69
	v_mul_f32_e32 v141, 0xc01d265f, v68
	v_exp_f32_e32 v163, v1
	s_cmp_le_i32 s96, 0
	s_cbranch_scc1 .Lp6ast_0
	global_store_dwordx4 v[146:147], v[164:167], off
.Lp6ast_0:
	v_pk_fma_f32 v[160:161], v[80:81], s[24:25], v[154:155] op_sel_hi:[1,0,1]
	v_pk_fma_f32 v[156:157], v[82:83], s[24:25], v[152:153] op_sel_hi:[1,0,1]
	v_exp_f32_e32 v164, v141
	v_mul_f32_e32 v141, 0xc01d265f, v69
	v_exp_f32_e32 v165, v141
	v_pk_add_f32 v[162:163], v[162:163], 1.0 op_sel_hi:[1,0]
	v_med3_f32 v160, v160, s64, v159
	v_rcp_f32_e32 v162, v162
	v_rcp_f32_e32 v163, v163
	v_pk_add_f32 v[164:165], v[164:165], 1.0 op_sel_hi:[1,0]
	v_med3_f32 v161, v161, s64, v159
	v_rcp_f32_e32 v164, v164
	v_rcp_f32_e32 v165, v165
	v_pk_mul_f32 v[70:71], v[70:71], v[162:163]
	v_med3_f32 v156, v156, s64, v159
	v_pk_mul_f32 v[70:71], v[160:161], v[70:71]
	v_pk_fma_f32 v[160:161], v[108:109], s[24:25], v[132:133] op_sel_hi:[1,0,1]
	v_med3_f32 v157, v157, s64, v159
	v_pk_mul_f32 v[68:69], v[68:69], v[164:165]
	v_min_f32_e32 v160, 0x40e00000, v160
	v_pk_mul_f32 v[156:157], v[156:157], v[68:69]
	v_pk_fma_f32 v[68:69], v[110:111], s[24:25], v[134:135] op_sel_hi:[1,0,1]
	v_min_f32_e32 v161, 0x40e00000, v161
	v_mul_f32_e32 v1, 0xc01d265f, v160
	v_min_f32_e32 v166, 0x40e00000, v68
	v_exp_f32_e32 v68, v1
	v_mul_f32_e32 v1, 0xc01d265f, v161
	v_min_f32_e32 v167, 0x40e00000, v69
	v_exp_f32_e32 v69, v1
	v_mul_f32_e32 v1, 0xc01d265f, v166
	v_exp_f32_e32 v168, v1
	v_mul_f32_e32 v1, 0xc01d265f, v167
	v_pk_add_f32 v[68:69], v[68:69], 1.0 op_sel_hi:[1,0]
	v_exp_f32_e32 v169, v1
	v_rcp_f32_e32 v68, v68
	v_rcp_f32_e32 v69, v69
	v_pk_fma_f32 v[164:165], v[76:77], s[24:25], v[150:151] op_sel_hi:[1,0,1]
	v_pk_add_f32 v[168:169], v[168:169], 1.0 op_sel_hi:[1,0]
	v_med3_f32 v164, v164, s64, v159
	v_med3_f32 v165, v165, s64, v159
	v_pk_mul_f32 v[68:69], v[160:161], v[68:69]
	v_rcp_f32_e32 v168, v168
	v_pk_mul_f32 v[160:161], v[164:165], v[68:69]
	v_mov_b32_e32 v68, 0
	v_rcp_f32_e32 v169, v169
	v_cvt_pk_fp8_f32 v68, v70, v71
	v_mov_b32_e32 v69, 0
	v_cvt_pk_fp8_f32 v69, v160, v161
	v_pk_fma_f32 v[162:163], v[78:79], s[24:25], v[148:149] op_sel_hi:[1,0,1]
	v_pk_mul_f32 v[70:71], v[166:167], v[168:169]
	v_med3_f32 v162, v162, s64, v159
	v_med3_f32 v163, v163, s64, v159
	v_cvt_pk_fp8_f32 v68, v156, v157 op_sel:[0,0,1]
	v_pk_fma_f32 v[156:157], v[104:105], s[24:25], v[136:137] op_sel_hi:[1,0,1]
	v_pk_mul_f32 v[70:71], v[162:163], v[70:71]
	v_min_f32_e32 v156, 0x40e00000, v156
	v_cvt_pk_fp8_f32 v69, v70, v71 op_sel:[0,0,1]
	v_pk_fma_f32 v[70:71], v[106:107], s[24:25], v[138:139] op_sel_hi:[1,0,1]
	v_min_f32_e32 v157, 0x40e00000, v157
	v_mul_f32_e32 v1, 0xc01d265f, v156
	v_min_f32_e32 v70, 0x40e00000, v70
	v_exp_f32_e32 v164, v1
	v_mul_f32_e32 v1, 0xc01d265f, v157
	v_min_f32_e32 v71, 0x40e00000, v71
	v_mul_f32_e32 v141, 0xc01d265f, v70
	v_exp_f32_e32 v165, v1
	v_exp_f32_e32 v166, v141
	v_mul_f32_e32 v141, 0xc01d265f, v71
	v_exp_f32_e32 v167, v141
	v_pk_add_f32 v[164:165], v[164:165], 1.0 op_sel_hi:[1,0]
	v_pk_fma_f32 v[162:163], v[72:73], s[24:25], v[154:155] op_sel_hi:[1,0,1]
	v_rcp_f32_e32 v164, v164
	v_rcp_f32_e32 v165, v165
	v_pk_add_f32 v[166:167], v[166:167], 1.0 op_sel_hi:[1,0]
	v_med3_f32 v162, v162, s64, v159
	v_rcp_f32_e32 v166, v166
	v_rcp_f32_e32 v167, v167
	v_med3_f32 v163, v163, s64, v159
	v_pk_mul_f32 v[156:157], v[156:157], v[164:165]
	v_pk_fma_f32 v[160:161], v[74:75], s[24:25], v[152:153] op_sel_hi:[1,0,1]
	v_pk_mul_f32 v[156:157], v[162:163], v[156:157]
	v_pk_fma_f32 v[162:163], v[100:101], s[24:25], v[132:133] op_sel_hi:[1,0,1]
	v_med3_f32 v160, v160, s64, v159
	v_med3_f32 v161, v161, s64, v159
	v_pk_mul_f32 v[70:71], v[70:71], v[166:167]
	v_min_f32_e32 v162, 0x40e00000, v162
	v_pk_mul_f32 v[160:161], v[160:161], v[70:71]
	v_pk_fma_f32 v[70:71], v[102:103], s[24:25], v[134:135] op_sel_hi:[1,0,1]
	v_min_f32_e32 v163, 0x40e00000, v163
	v_mul_f32_e32 v1, 0xc01d265f, v162
	v_min_f32_e32 v168, 0x40e00000, v70
	v_exp_f32_e32 v70, v1
	v_mul_f32_e32 v1, 0xc01d265f, v163
	v_min_f32_e32 v169, 0x40e00000, v71
	v_exp_f32_e32 v71, v1
	v_mul_f32_e32 v1, 0xc01d265f, v168
	v_exp_f32_e32 v170, v1
	v_mul_f32_e32 v1, 0xc01d265f, v169
	v_exp_f32_e32 v171, v1
	v_pk_add_f32 v[70:71], v[70:71], 1.0 op_sel_hi:[1,0]
	v_pk_fma_f32 v[166:167], v[28:29], s[24:25], v[150:151] op_sel_hi:[1,0,1]
	v_rcp_f32_e32 v70, v70
	v_rcp_f32_e32 v71, v71
	v_pk_add_f32 v[170:171], v[170:171], 1.0 op_sel_hi:[1,0]
	v_med3_f32 v166, v166, s64, v159
	v_med3_f32 v167, v167, s64, v159
	v_rcp_f32_e32 v170, v170
	v_rcp_f32_e32 v171, v171
	v_pk_mul_f32 v[70:71], v[162:163], v[70:71]
	v_pk_fma_f32 v[164:165], v[30:31], s[24:25], v[148:149] op_sel_hi:[1,0,1]
	v_pk_mul_f32 v[162:163], v[166:167], v[70:71]
	v_mov_b32_e32 v70, 0
	v_mov_b32_e32 v71, 0
	v_cvt_pk_fp8_f32 v70, v156, v157
	v_cvt_pk_fp8_f32 v71, v162, v163
	v_med3_f32 v164, v164, s64, v159
	v_med3_f32 v165, v165, s64, v159
	v_pk_mul_f32 v[156:157], v[168:169], v[170:171]
	v_cvt_pk_fp8_f32 v70, v160, v161 op_sel:[0,0,1]
	v_pk_mul_f32 v[156:157], v[164:165], v[156:157]
	v_pk_fma_f32 v[160:161], v[32:33], s[24:25], v[154:155] op_sel_hi:[1,0,1]
	v_cvt_pk_fp8_f32 v71, v156, v157 op_sel:[0,0,1]
	v_add_co_u32_e32 v156, vcc, s5, v146
	v_permlane16_swap_b32_e32 v68, v70
	v_permlane16_swap_b32_e32 v69, v71
	v_addc_co_u32_e32 v157, vcc, 0, v147, vcc
	s_cmp_le_i32 s96, 32
	s_cbranch_scc1 .Lp6ast_1
	global_store_dwordx4 v[156:157], v[68:71], off
.Lp6ast_1:
	v_med3_f32 v160, v160, s64, v159
	v_med3_f32 v161, v161, s64, v159
	v_pk_fma_f32 v[70:71], v[64:65], s[24:25], v[136:137] op_sel_hi:[1,0,1]
	v_pk_fma_f32 v[68:69], v[66:67], s[24:25], v[138:139] op_sel_hi:[1,0,1]
	v_min_f32_e32 v70, 0x40e00000, v70
	v_min_f32_e32 v71, 0x40e00000, v71
	v_mul_f32_e32 v1, 0xc01d265f, v70
	v_min_f32_e32 v68, 0x40e00000, v68
	v_exp_f32_e32 v162, v1
	v_mul_f32_e32 v1, 0xc01d265f, v71
	v_min_f32_e32 v69, 0x40e00000, v69
	v_mul_f32_e32 v141, 0xc01d265f, v68
	v_exp_f32_e32 v163, v1
	v_exp_f32_e32 v164, v141
	v_mul_f32_e32 v141, 0xc01d265f, v69
	v_exp_f32_e32 v165, v141
	v_pk_add_f32 v[162:163], v[162:163], 1.0 op_sel_hi:[1,0]
	v_pk_fma_f32 v[156:157], v[34:35], s[24:25], v[152:153] op_sel_hi:[1,0,1]
	v_rcp_f32_e32 v162, v162
	v_rcp_f32_e32 v163, v163
	v_pk_add_f32 v[164:165], v[164:165], 1.0 op_sel_hi:[1,0]
	v_med3_f32 v156, v156, s64, v159
	v_rcp_f32_e32 v164, v164
	v_rcp_f32_e32 v165, v165
	v_pk_mul_f32 v[70:71], v[70:71], v[162:163]
	v_med3_f32 v157, v157, s64, v159
	v_pk_mul_f32 v[70:71], v[160:161], v[70:71]
	v_pk_fma_f32 v[160:161], v[60:61], s[24:25], v[132:133] op_sel_hi:[1,0,1]
	v_pk_mul_f32 v[68:69], v[68:69], v[164:165]
	v_min_f32_e32 v160, 0x40e00000, v160
	v_pk_mul_f32 v[156:157], v[156:157], v[68:69]
	v_pk_fma_f32 v[68:69], v[62:63], s[24:25], v[134:135] op_sel_hi:[1,0,1]
	v_min_f32_e32 v161, 0x40e00000, v161
	v_mul_f32_e32 v1, 0xc01d265f, v160
	v_min_f32_e32 v166, 0x40e00000, v68
	v_exp_f32_e32 v68, v1
	v_mul_f32_e32 v1, 0xc01d265f, v161
	v_min_f32_e32 v167, 0x40e00000, v69
	v_exp_f32_e32 v69, v1
	v_mul_f32_e32 v1, 0xc01d265f, v166
	v_exp_f32_e32 v168, v1
	v_mul_f32_e32 v1, 0xc01d265f, v167
	v_pk_add_f32 v[68:69], v[68:69], 1.0 op_sel_hi:[1,0]
	v_exp_f32_e32 v169, v1
	v_rcp_f32_e32 v68, v68
	v_rcp_f32_e32 v69, v69
	v_pk_fma_f32 v[164:165], v[232:233], s[24:25], v[150:151] op_sel_hi:[1,0,1]
	v_pk_add_f32 v[168:169], v[168:169], 1.0 op_sel_hi:[1,0]
	v_med3_f32 v164, v164, s64, v159
	v_med3_f32 v165, v165, s64, v159
	v_pk_mul_f32 v[68:69], v[160:161], v[68:69]
	v_rcp_f32_e32 v168, v168
	v_pk_mul_f32 v[160:161], v[164:165], v[68:69]
	v_mov_b32_e32 v68, 0
	v_rcp_f32_e32 v169, v169
	v_cvt_pk_fp8_f32 v68, v70, v71
	v_mov_b32_e32 v69, 0
	v_cvt_pk_fp8_f32 v69, v160, v161
	v_pk_fma_f32 v[162:163], v[234:235], s[24:25], v[148:149] op_sel_hi:[1,0,1]
	v_pk_mul_f32 v[70:71], v[166:167], v[168:169]
	v_med3_f32 v162, v162, s64, v159
	v_med3_f32 v163, v163, s64, v159
	v_cvt_pk_fp8_f32 v68, v156, v157 op_sel:[0,0,1]
	v_pk_fma_f32 v[156:157], v[56:57], s[24:25], v[136:137] op_sel_hi:[1,0,1]
	v_pk_mul_f32 v[70:71], v[162:163], v[70:71]
	v_min_f32_e32 v156, 0x40e00000, v156
	v_cvt_pk_fp8_f32 v69, v70, v71 op_sel:[0,0,1]
	v_pk_fma_f32 v[70:71], v[58:59], s[24:25], v[138:139] op_sel_hi:[1,0,1]
	v_min_f32_e32 v157, 0x40e00000, v157
	v_mul_f32_e32 v1, 0xc01d265f, v156
	v_min_f32_e32 v70, 0x40e00000, v70
	v_exp_f32_e32 v164, v1
	v_mul_f32_e32 v1, 0xc01d265f, v157
	v_min_f32_e32 v71, 0x40e00000, v71
	v_mul_f32_e32 v141, 0xc01d265f, v70
	v_exp_f32_e32 v165, v1
	v_exp_f32_e32 v166, v141
	v_mul_f32_e32 v141, 0xc01d265f, v71
	v_exp_f32_e32 v167, v141
	v_pk_add_f32 v[164:165], v[164:165], 1.0 op_sel_hi:[1,0]
	v_pk_fma_f32 v[162:163], v[24:25], s[24:25], v[154:155] op_sel_hi:[1,0,1]
	v_rcp_f32_e32 v164, v164
	v_rcp_f32_e32 v165, v165
	v_pk_add_f32 v[166:167], v[166:167], 1.0 op_sel_hi:[1,0]
	v_med3_f32 v162, v162, s64, v159
	v_rcp_f32_e32 v166, v166
	v_rcp_f32_e32 v167, v167
	v_med3_f32 v163, v163, s64, v159
	v_pk_mul_f32 v[156:157], v[156:157], v[164:165]
	v_pk_fma_f32 v[160:161], v[26:27], s[24:25], v[152:153] op_sel_hi:[1,0,1]
	v_pk_mul_f32 v[156:157], v[162:163], v[156:157]
	v_pk_fma_f32 v[162:163], v[52:53], s[24:25], v[132:133] op_sel_hi:[1,0,1]
	v_med3_f32 v160, v160, s64, v159
	v_med3_f32 v161, v161, s64, v159
	v_pk_mul_f32 v[70:71], v[70:71], v[166:167]
	v_min_f32_e32 v162, 0x40e00000, v162
	v_pk_mul_f32 v[160:161], v[160:161], v[70:71]
	v_pk_fma_f32 v[70:71], v[54:55], s[24:25], v[134:135] op_sel_hi:[1,0,1]
	v_min_f32_e32 v163, 0x40e00000, v163
	v_mul_f32_e32 v1, 0xc01d265f, v162
	v_min_f32_e32 v168, 0x40e00000, v70
	v_exp_f32_e32 v70, v1
	v_mul_f32_e32 v1, 0xc01d265f, v163
	v_min_f32_e32 v169, 0x40e00000, v71
	v_exp_f32_e32 v71, v1
	v_mul_f32_e32 v1, 0xc01d265f, v168
	v_exp_f32_e32 v170, v1
	v_mul_f32_e32 v1, 0xc01d265f, v169
	v_exp_f32_e32 v171, v1
	v_pk_add_f32 v[70:71], v[70:71], 1.0 op_sel_hi:[1,0]
	v_pk_fma_f32 v[166:167], v[20:21], s[24:25], v[150:151] op_sel_hi:[1,0,1]
	v_rcp_f32_e32 v70, v70
	v_rcp_f32_e32 v71, v71
	v_pk_add_f32 v[170:171], v[170:171], 1.0 op_sel_hi:[1,0]
	v_med3_f32 v166, v166, s64, v159
	v_med3_f32 v167, v167, s64, v159
	v_rcp_f32_e32 v170, v170
	v_rcp_f32_e32 v171, v171
	v_pk_mul_f32 v[70:71], v[162:163], v[70:71]
	v_pk_fma_f32 v[164:165], v[22:23], s[24:25], v[148:149] op_sel_hi:[1,0,1]
	v_pk_mul_f32 v[162:163], v[166:167], v[70:71]
	v_mov_b32_e32 v70, 0
	v_mov_b32_e32 v71, 0
	v_cvt_pk_fp8_f32 v70, v156, v157
	v_cvt_pk_fp8_f32 v71, v162, v163
	v_med3_f32 v164, v164, s64, v159
	v_med3_f32 v165, v165, s64, v159
	v_pk_mul_f32 v[156:157], v[168:169], v[170:171]
	v_cvt_pk_fp8_f32 v70, v160, v161 op_sel:[0,0,1]
	v_pk_mul_f32 v[156:157], v[164:165], v[156:157]
	s_mov_b32 s5, 0x40000
	v_cvt_pk_fp8_f32 v71, v156, v157 op_sel:[0,0,1]
	v_add_co_u32_e32 v156, vcc, s5, v146
	v_permlane16_swap_b32_e32 v68, v70
	v_permlane16_swap_b32_e32 v69, v71
	v_addc_co_u32_e32 v157, vcc, 0, v147, vcc
	s_cmp_le_i32 s96, 128
	s_cbranch_scc1 .Lp6ast_2
	global_store_dwordx4 v[156:157], v[68:71], off
.Lp6ast_2:
	v_pk_fma_f32 v[160:161], v[16:17], s[24:25], v[154:155] op_sel_hi:[1,0,1]
	v_pk_fma_f32 v[156:157], v[18:19], s[24:25], v[152:153] op_sel_hi:[1,0,1]
	v_pk_fma_f32 v[70:71], v[48:49], s[24:25], v[136:137] op_sel_hi:[1,0,1]
	v_pk_fma_f32 v[68:69], v[50:51], s[24:25], v[138:139] op_sel_hi:[1,0,1]
	v_min_f32_e32 v70, 0x40e00000, v70
	v_min_f32_e32 v71, 0x40e00000, v71
	v_mul_f32_e32 v1, 0xc01d265f, v70
	v_min_f32_e32 v68, 0x40e00000, v68
	v_exp_f32_e32 v162, v1
	v_mul_f32_e32 v1, 0xc01d265f, v71
	v_min_f32_e32 v69, 0x40e00000, v69
	v_mul_f32_e32 v141, 0xc01d265f, v68
	v_exp_f32_e32 v163, v1
	v_exp_f32_e32 v164, v141
	v_mul_f32_e32 v141, 0xc01d265f, v69
	v_exp_f32_e32 v165, v141
	v_pk_add_f32 v[162:163], v[162:163], 1.0 op_sel_hi:[1,0]
	v_med3_f32 v160, v160, s64, v159
	v_rcp_f32_e32 v162, v162
	v_rcp_f32_e32 v163, v163
	v_pk_add_f32 v[164:165], v[164:165], 1.0 op_sel_hi:[1,0]
	v_med3_f32 v161, v161, s64, v159
	v_rcp_f32_e32 v164, v164
	v_rcp_f32_e32 v165, v165
	v_pk_mul_f32 v[70:71], v[70:71], v[162:163]
	v_med3_f32 v156, v156, s64, v159
	v_pk_mul_f32 v[70:71], v[160:161], v[70:71]
	v_pk_fma_f32 v[160:161], v[44:45], s[24:25], v[132:133] op_sel_hi:[1,0,1]
	v_med3_f32 v157, v157, s64, v159
	v_pk_mul_f32 v[68:69], v[68:69], v[164:165]
	v_min_f32_e32 v160, 0x40e00000, v160
	v_pk_mul_f32 v[156:157], v[156:157], v[68:69]
	v_pk_fma_f32 v[68:69], v[46:47], s[24:25], v[134:135] op_sel_hi:[1,0,1]
	v_min_f32_e32 v161, 0x40e00000, v161
	v_mul_f32_e32 v1, 0xc01d265f, v160
	v_min_f32_e32 v166, 0x40e00000, v68
	v_exp_f32_e32 v68, v1
	v_mul_f32_e32 v1, 0xc01d265f, v161
	v_min_f32_e32 v167, 0x40e00000, v69
	v_exp_f32_e32 v69, v1
	v_mul_f32_e32 v1, 0xc01d265f, v166
	v_exp_f32_e32 v168, v1
	v_mul_f32_e32 v1, 0xc01d265f, v167
	v_exp_f32_e32 v169, v1
	v_pk_add_f32 v[68:69], v[68:69], 1.0 op_sel_hi:[1,0]
	v_pk_fma_f32 v[164:165], v[12:13], s[24:25], v[150:151] op_sel_hi:[1,0,1]
	v_rcp_f32_e32 v68, v68
	v_rcp_f32_e32 v69, v69
	v_pk_add_f32 v[168:169], v[168:169], 1.0 op_sel_hi:[1,0]
	v_med3_f32 v164, v164, s64, v159
	v_med3_f32 v165, v165, s64, v159
	v_rcp_f32_e32 v168, v168
	v_rcp_f32_e32 v169, v169
	v_pk_mul_f32 v[68:69], v[160:161], v[68:69]
	v_pk_fma_f32 v[162:163], v[14:15], s[24:25], v[148:149] op_sel_hi:[1,0,1]
	v_pk_mul_f32 v[160:161], v[164:165], v[68:69]
	v_mov_b32_e32 v69, 0
	v_cvt_pk_fp8_f32 v69, v160, v161
	v_mov_b32_e32 v68, 0
	v_med3_f32 v162, v162, s64, v159
	v_med3_f32 v163, v163, s64, v159
	v_cvt_pk_fp8_f32 v68, v70, v71
	v_pk_mul_f32 v[70:71], v[166:167], v[168:169]
	v_pk_fma_f32 v[136:137], v[40:41], s[24:25], v[136:137] op_sel_hi:[1,0,1]
	v_pk_mul_f32 v[70:71], v[162:163], v[70:71]
	v_cvt_pk_fp8_f32 v68, v156, v157 op_sel:[0,0,1]
	v_cvt_pk_fp8_f32 v69, v70, v71 op_sel:[0,0,1]
	v_pk_fma_f32 v[70:71], v[42:43], s[24:25], v[138:139] op_sel_hi:[1,0,1]
	v_min_f32_e32 v136, 0x40e00000, v136
	v_min_f32_e32 v70, 0x40e00000, v70
	v_min_f32_e32 v71, 0x40e00000, v71
	v_mul_f32_e32 v141, 0xc01d265f, v70
	v_exp_f32_e32 v156, v141
	v_mul_f32_e32 v141, 0xc01d265f, v71
	v_exp_f32_e32 v157, v141
	v_min_f32_e32 v137, 0x40e00000, v137
	v_mul_f32_e32 v1, 0xc01d265f, v136
	v_pk_fma_f32 v[138:139], v[10:11], s[24:25], v[152:153] op_sel_hi:[1,0,1]
	v_pk_fma_f32 v[152:153], v[8:9], s[24:25], v[154:155] op_sel_hi:[1,0,1]
	v_exp_f32_e32 v154, v1
	v_mul_f32_e32 v1, 0xc01d265f, v137
	v_pk_add_f32 v[156:157], v[156:157], 1.0 op_sel_hi:[1,0]
	v_exp_f32_e32 v155, v1
	v_rcp_f32_e32 v156, v156
	v_rcp_f32_e32 v157, v157
	v_pk_fma_f32 v[132:133], v[36:37], s[24:25], v[132:133] op_sel_hi:[1,0,1]
	v_pk_add_f32 v[154:155], v[154:155], 1.0 op_sel_hi:[1,0]
	v_med3_f32 v138, v138, s64, v159
	v_med3_f32 v139, v139, s64, v159
	v_pk_mul_f32 v[70:71], v[70:71], v[156:157]
	v_min_f32_e32 v132, 0x40e00000, v132
	v_rcp_f32_e32 v154, v154
	v_rcp_f32_e32 v155, v155
	v_pk_mul_f32 v[138:139], v[138:139], v[70:71]
	v_pk_fma_f32 v[70:71], v[38:39], s[24:25], v[134:135] op_sel_hi:[1,0,1]
	v_min_f32_e32 v133, 0x40e00000, v133
	v_mul_f32_e32 v1, 0xc01d265f, v132
	v_pk_fma_f32 v[134:135], v[6:7], s[24:25], v[148:149] op_sel_hi:[1,0,1]
	v_pk_fma_f32 v[148:149], v[4:5], s[24:25], v[150:151] op_sel_hi:[1,0,1]
	v_min_f32_e32 v150, 0x40e00000, v70
	v_exp_f32_e32 v70, v1
	v_mul_f32_e32 v1, 0xc01d265f, v133
	v_min_f32_e32 v151, 0x40e00000, v71
	v_exp_f32_e32 v71, v1
	v_med3_f32 v152, v152, s64, v159
	v_med3_f32 v153, v153, s64, v159
	v_pk_mul_f32 v[136:137], v[136:137], v[154:155]
	v_mul_f32_e32 v1, 0xc01d265f, v150
	v_pk_mul_f32 v[136:137], v[152:153], v[136:137]
	v_exp_f32_e32 v152, v1
	v_mul_f32_e32 v1, 0xc01d265f, v151
	v_exp_f32_e32 v153, v1
	v_pk_add_f32 v[70:71], v[70:71], 1.0 op_sel_hi:[1,0]
	v_med3_f32 v148, v148, s64, v159
	v_rcp_f32_e32 v70, v70
	v_rcp_f32_e32 v71, v71
	v_pk_add_f32 v[152:153], v[152:153], 1.0 op_sel_hi:[1,0]
	v_med3_f32 v149, v149, s64, v159
	v_rcp_f32_e32 v152, v152
	v_rcp_f32_e32 v153, v153
	v_pk_mul_f32 v[70:71], v[132:133], v[70:71]
	v_med3_f32 v134, v134, s64, v159
	v_pk_mul_f32 v[132:133], v[148:149], v[70:71]
	v_mov_b32_e32 v70, 0
	v_mov_b32_e32 v71, 0
	v_cvt_pk_fp8_f32 v70, v136, v137
	v_cvt_pk_fp8_f32 v71, v132, v133
	v_med3_f32 v135, v135, s64, v159
	v_pk_mul_f32 v[132:133], v[150:151], v[152:153]
	v_cvt_pk_fp8_f32 v70, v138, v139 op_sel:[0,0,1]
	v_pk_mul_f32 v[132:133], v[134:135], v[132:133]
	s_nop 0
	v_permlane16_swap_b32_e32 v68, v70
	v_cvt_pk_fp8_f32 v71, v132, v133 op_sel:[0,0,1]
	v_add_co_u32_e32 v132, vcc, 0x50000, v146
	s_nop 0
	v_permlane16_swap_b32_e32 v69, v71
	v_addc_co_u32_e32 v133, vcc, 0, v147, vcc
	s_andn2_b64 vcc, exec, s[36:37]
	s_cmp_le_i32 s96, 160
	s_cbranch_scc1 .Lp6ast_3
	global_store_dwordx4 v[132:133], v[68:71], off
.Lp6ast_3:
	s_cbranch_vccnz .LBB0_803
	ds_read_b128 v[0:3], v253
	s_andn2_b64 vcc, exec, s[20:21]
	s_cbranch_vccnz .LBB0_802
	s_barrier
	s_branch .LBB0_802

.LBB0_886:
	v_and_b32_e32 v5, 15, v4
	s_add_i32 s0, 0, 0x21000
	v_or_b32_e32 v6, s53, v5
	v_lshl_add_u32 v253, v4, 4, s0
	v_and_b32_e32 v7, 48, v4
	v_lshlrev_b32_e32 v8, 6, v6
	s_movk_i32 s0, 0x3c0
	v_and_or_b32 v8, v8, s0, v7
	v_lshlrev_b32_e32 v4, 2, v4
	s_add_u32 s0, s18, 0x80
	v_lshl_or_b32 v5, v5, 6, v7
	v_and_b32_e32 v4, 32, v4
	s_addc_u32 s1, s19, 0
	v_bitop3_b32 v158, v5, s56, v4 bitop3:0xde
	s_waitcnt vmcnt(2)
	s_barrier
	s_add_i32 m0, s7, 0x18000
	v_lshl_add_u64 v[4:5], s[0:1], 0, v[140:141]
	v_lshlrev_b32_e32 v6, 2, v6
	global_load_lds_dwordx4 v[4:5], off
	s_add_i32 m0, s7, 0x1a000
	v_and_b32_e32 v6, 32, v6
	v_lshl_add_u64 v[4:5], s[0:1], 0, v[142:143]
	s_add_u32 s0, s90, 0x12800080
	v_bitop3_b32 v6, v8, s55, v6 bitop3:0xde
	s_addc_u32 s1, s91, 0
	s_add_i32 s55, s7, 0x8000
	global_load_lds_dwordx4 v[4:5], off
	s_mov_b32 m0, s55
	v_lshl_add_u64 v[4:5], s[0:1], 0, v[0:1]
	s_add_i32 s56, s7, 0xa000
	global_load_lds_dwordx4 v[4:5], off
	v_lshl_add_u64 v[4:5], s[0:1], 0, v[144:145]
	s_add_u32 s0, s18, 0x40080
	s_mov_b32 m0, s56
	s_addc_u32 s1, s19, 0
	global_load_lds_dwordx4 v[4:5], off
	s_add_i32 m0, s7, 0x1c000
	v_lshl_add_u64 v[4:5], s[0:1], 0, v[140:141]
	global_load_lds_dwordx4 v[4:5], off
	v_lshl_add_u64 v[4:5], s[0:1], 0, v[142:143]
	s_add_i32 m0, s7, 0x1e000
	v_readlane_b32 s0, v255, 25
	global_load_lds_dwordx4 v[4:5], off
	s_waitcnt vmcnt(6)
	s_cmpk_lt_u32 s0, 0x100
	s_cselect_b64 s[22:23], -1, 0
	s_add_i32 s57, 0, 0x10000
	s_add_i32 s61, 0, 0x14000
	v_add_u32_e32 v143, 0, v6
	v_mov_b32_e32 v145, 0x7f7f7f7f
	s_mov_b32 s24, 0x3c800000
	s_mov_b32 s62, 0xc0c00000
	s_mov_b32 s63, 0x40000
	v_mov_b32_e32 v159, 0x41000000
	v_mov_b32_e32 v4, v141
	v_mov_b32_e32 v5, v141
	v_mov_b32_e32 v6, v141
	v_mov_b32_e32 v7, v141
	v_mov_b32_e32 v8, v141
	v_mov_b32_e32 v9, v141
	v_mov_b32_e32 v10, v141
	v_mov_b32_e32 v11, v141
	v_mov_b32_e32 v12, v141
	v_mov_b32_e32 v13, v141
	v_mov_b32_e32 v14, v141
	v_mov_b32_e32 v15, v141
	v_mov_b32_e32 v16, v141
	v_mov_b32_e32 v17, v141
	v_mov_b32_e32 v18, v141
	v_mov_b32_e32 v19, v141
	v_mov_b32_e32 v20, v141
	v_mov_b32_e32 v21, v141
	v_mov_b32_e32 v22, v141
	v_mov_b32_e32 v23, v141
	v_mov_b32_e32 v24, v141
	v_mov_b32_e32 v25, v141
	v_mov_b32_e32 v26, v141
	v_mov_b32_e32 v27, v141
	v_mov_b32_e32 v232, v141
	v_mov_b32_e32 v233, v141
	v_mov_b32_e32 v234, v141
	v_mov_b32_e32 v235, v141
	v_mov_b32_e32 v32, v141
	v_mov_b32_e32 v33, v141
	v_mov_b32_e32 v34, v141
	v_mov_b32_e32 v35, v141
	v_mov_b32_e32 v36, v141
	v_mov_b32_e32 v37, v141
	v_mov_b32_e32 v38, v141
	v_mov_b32_e32 v39, v141
	v_mov_b32_e32 v40, v141
	v_mov_b32_e32 v41, v141
	v_mov_b32_e32 v42, v141
	v_mov_b32_e32 v43, v141
	v_mov_b32_e32 v44, v141
	v_mov_b32_e32 v45, v141
	v_mov_b32_e32 v46, v141
	v_mov_b32_e32 v47, v141
	v_mov_b32_e32 v48, v141
	v_mov_b32_e32 v49, v141
	v_mov_b32_e32 v50, v141
	v_mov_b32_e32 v51, v141
	v_mov_b32_e32 v52, v141
	v_mov_b32_e32 v53, v141
	v_mov_b32_e32 v54, v141
	v_mov_b32_e32 v55, v141
	v_mov_b32_e32 v56, v141
	v_mov_b32_e32 v57, v141
	v_mov_b32_e32 v58, v141
	v_mov_b32_e32 v59, v141
	v_mov_b32_e32 v60, v141
	v_mov_b32_e32 v61, v141
	v_mov_b32_e32 v62, v141
	v_mov_b32_e32 v63, v141
	v_mov_b32_e32 v64, v141
	v_mov_b32_e32 v65, v141
	v_mov_b32_e32 v66, v141
	v_mov_b32_e32 v67, v141
	v_mov_b32_e32 v28, v141
	v_mov_b32_e32 v29, v141
	v_mov_b32_e32 v30, v141
	v_mov_b32_e32 v31, v141
	v_mov_b32_e32 v72, v141
	v_mov_b32_e32 v73, v141
	v_mov_b32_e32 v74, v141
	v_mov_b32_e32 v75, v141
	v_mov_b32_e32 v76, v141
	v_mov_b32_e32 v77, v141
	v_mov_b32_e32 v78, v141
	v_mov_b32_e32 v79, v141
	v_mov_b32_e32 v80, v141
	v_mov_b32_e32 v81, v141
	v_mov_b32_e32 v82, v141
	v_mov_b32_e32 v83, v141
	v_mov_b32_e32 v84, v141
	v_mov_b32_e32 v85, v141
	v_mov_b32_e32 v86, v141
	v_mov_b32_e32 v87, v141
	v_mov_b32_e32 v88, v141
	v_mov_b32_e32 v89, v141
	v_mov_b32_e32 v90, v141
	v_mov_b32_e32 v91, v141
	v_mov_b32_e32 v92, v141
	v_mov_b32_e32 v93, v141
	v_mov_b32_e32 v94, v141
	v_mov_b32_e32 v95, v141
	v_mov_b32_e32 v96, v141
	v_mov_b32_e32 v97, v141
	v_mov_b32_e32 v98, v141
	v_mov_b32_e32 v99, v141
	v_mov_b32_e32 v100, v141
	v_mov_b32_e32 v101, v141
	v_mov_b32_e32 v102, v141
	v_mov_b32_e32 v103, v141
	v_mov_b32_e32 v104, v141
	v_mov_b32_e32 v105, v141
	v_mov_b32_e32 v106, v141
	v_mov_b32_e32 v107, v141
	v_mov_b32_e32 v108, v141
	v_mov_b32_e32 v109, v141
	v_mov_b32_e32 v110, v141
	v_mov_b32_e32 v111, v141
	v_mov_b32_e32 v112, v141
	v_mov_b32_e32 v113, v141
	v_mov_b32_e32 v114, v141
	v_mov_b32_e32 v115, v141
	v_mov_b32_e32 v116, v141
	v_mov_b32_e32 v117, v141
	v_mov_b32_e32 v118, v141
	v_mov_b32_e32 v119, v141
	v_mov_b32_e32 v120, v141
	v_mov_b32_e32 v121, v141
	v_mov_b32_e32 v122, v141
	v_mov_b32_e32 v123, v141
	v_mov_b32_e32 v124, v141
	v_mov_b32_e32 v125, v141
	v_mov_b32_e32 v126, v141
	v_mov_b32_e32 v127, v141
	v_mov_b32_e32 v128, v141
	v_mov_b32_e32 v129, v141
	v_mov_b32_e32 v130, v141
	v_mov_b32_e32 v131, v141
	s_barrier
	s_mov_b32 s97, 0x7fffffff
	s_branch .LBB0_889
.LBB0_887:
	s_mov_b32 s97, s66
	v_mov_b32_e32 v4, 0
	s_waitcnt lgkmcnt(0)
	v_mov_b32_e32 v144, v1
	s_mov_b32 s2, s64
	s_mov_b32 s6, s28
	s_mov_b32 s4, s26
	s_mov_b64 s[18:19], s[0:1]
	s_mov_b32 s60, s67
	v_mov_b32_e32 v5, v4
	v_mov_b32_e32 v6, v4
	v_mov_b32_e32 v7, v4
	v_mov_b32_e32 v8, v4
	v_mov_b32_e32 v9, v4
	v_mov_b32_e32 v10, v4
	v_mov_b32_e32 v11, v4
	v_mov_b32_e32 v12, v4
	v_mov_b32_e32 v13, v4
	v_mov_b32_e32 v14, v4
	v_mov_b32_e32 v15, v4
	v_mov_b32_e32 v16, v4
	v_mov_b32_e32 v17, v4
	v_mov_b32_e32 v18, v4
	v_mov_b32_e32 v19, v4
	v_mov_b32_e32 v20, v4
	v_mov_b32_e32 v21, v4
	v_mov_b32_e32 v22, v4
	v_mov_b32_e32 v23, v4
	v_mov_b32_e32 v24, v4
	v_mov_b32_e32 v25, v4
	v_mov_b32_e32 v26, v4
	v_mov_b32_e32 v27, v4
	v_mov_b32_e32 v232, v4
	v_mov_b32_e32 v233, v4
	v_mov_b32_e32 v234, v4
	v_mov_b32_e32 v235, v4
	v_mov_b32_e32 v32, v4
	v_mov_b32_e32 v33, v4
	v_mov_b32_e32 v34, v4
	v_mov_b32_e32 v35, v4
	v_mov_b32_e32 v36, v4
	v_mov_b32_e32 v37, v4
	v_mov_b32_e32 v38, v4
	v_mov_b32_e32 v39, v4
	v_mov_b32_e32 v40, v4
	v_mov_b32_e32 v41, v4
	v_mov_b32_e32 v42, v4
	v_mov_b32_e32 v43, v4
	v_mov_b32_e32 v44, v4
	v_mov_b32_e32 v45, v4
	v_mov_b32_e32 v46, v4
	v_mov_b32_e32 v47, v4
	v_mov_b32_e32 v48, v4
	v_mov_b32_e32 v49, v4
	v_mov_b32_e32 v50, v4
	v_mov_b32_e32 v51, v4
	v_mov_b32_e32 v52, v4
	v_mov_b32_e32 v53, v4
	v_mov_b32_e32 v54, v4
	v_mov_b32_e32 v55, v4
	v_mov_b32_e32 v56, v4
	v_mov_b32_e32 v57, v4
	v_mov_b32_e32 v58, v4
	v_mov_b32_e32 v59, v4
	v_mov_b32_e32 v60, v4
	v_mov_b32_e32 v61, v4
	v_mov_b32_e32 v62, v4
	v_mov_b32_e32 v63, v4
	v_mov_b32_e32 v64, v4
	v_mov_b32_e32 v65, v4
	v_mov_b32_e32 v66, v4
	v_mov_b32_e32 v67, v4
	v_mov_b32_e32 v28, v4
	v_mov_b32_e32 v29, v4
	v_mov_b32_e32 v30, v4
	v_mov_b32_e32 v31, v4
	v_mov_b32_e32 v72, v4
	v_mov_b32_e32 v73, v4
	v_mov_b32_e32 v74, v4
	v_mov_b32_e32 v75, v4
	v_mov_b32_e32 v76, v4
	v_mov_b32_e32 v77, v4
	v_mov_b32_e32 v78, v4
	v_mov_b32_e32 v79, v4
	v_mov_b32_e32 v80, v4
	v_mov_b32_e32 v81, v4
	v_mov_b32_e32 v82, v4
	v_mov_b32_e32 v83, v4
	v_mov_b32_e32 v84, v4
	v_mov_b32_e32 v85, v4
	v_mov_b32_e32 v86, v4
	v_mov_b32_e32 v87, v4
	v_mov_b32_e32 v88, v4
	v_mov_b32_e32 v89, v4
	v_mov_b32_e32 v90, v4
	v_mov_b32_e32 v91, v4
	v_mov_b32_e32 v92, v4
	v_mov_b32_e32 v93, v4
	v_mov_b32_e32 v94, v4
	v_mov_b32_e32 v95, v4
	v_mov_b32_e32 v96, v4
	v_mov_b32_e32 v97, v4
	v_mov_b32_e32 v98, v4
	v_mov_b32_e32 v99, v4
	v_mov_b32_e32 v100, v4
	v_mov_b32_e32 v101, v4
	v_mov_b32_e32 v102, v4
	v_mov_b32_e32 v103, v4
	v_mov_b32_e32 v104, v4
	v_mov_b32_e32 v105, v4
	v_mov_b32_e32 v106, v4
	v_mov_b32_e32 v107, v4
	v_mov_b32_e32 v108, v4
	v_mov_b32_e32 v109, v4
	v_mov_b32_e32 v110, v4
	v_mov_b32_e32 v111, v4
	v_mov_b32_e32 v112, v4
	v_mov_b32_e32 v113, v4
	v_mov_b32_e32 v114, v4
	v_mov_b32_e32 v115, v4
	v_mov_b32_e32 v116, v4
	v_mov_b32_e32 v117, v4
	v_mov_b32_e32 v118, v4
	v_mov_b32_e32 v119, v4
	v_mov_b32_e32 v120, v4
	v_mov_b32_e32 v121, v4
	v_mov_b32_e32 v122, v4
	v_mov_b32_e32 v123, v4
	v_mov_b32_e32 v124, v4
	v_mov_b32_e32 v125, v4
	v_mov_b32_e32 v126, v4
	v_mov_b32_e32 v127, v4
	v_mov_b32_e32 v128, v4
	v_mov_b32_e32 v129, v4
	v_mov_b32_e32 v130, v4
	v_mov_b32_e32 v131, v4

.LBB0_922:
	s_sub_i32 s96, s97, s53
	s_lshl_b32 s5, s6, 7
	v_mbcnt_lo_u32_b32 v1, -1, 0
	v_mbcnt_hi_u32_b32 v1, -1, v1
	s_or_b32 s5, s5, s54
	v_ashrrev_i32_e32 v141, 4, v1
	v_lshl_add_u32 v146, v141, 3, s5
	s_ashr_i32 s5, s4, 31
	v_readlane_b32 s72, v255, 31
	s_lshl_b64 s[38:39], s[4:5], 13
	v_readlane_b32 s76, v255, 35
	v_readlane_b32 s77, v255, 36
	s_add_u32 s40, s76, s38
	v_readlane_b32 s80, v255, 39
	s_addc_u32 s41, s77, s39
	v_ashrrev_i32_e32 v147, 31, v146
	v_readlane_b32 s81, v255, 40
	v_lshlrev_b64 v[68:69], 2, v[146:147]
	s_add_u32 s38, s80, s38
	v_lshl_add_u64 v[70:71], s[40:41], 0, v[68:69]
	s_addc_u32 s39, s81, s39
	global_load_dwordx4 v[136:139], v[70:71], off
	global_load_dwordx4 v[132:135], v[70:71], off offset:16
	v_lshl_add_u64 v[148:149], s[38:39], 0, v[68:69]
	global_load_dwordx4 v[68:71], v[148:149], off
	global_load_dwordx4 v[160:163], v[148:149], off offset:16
	v_and_b32_e32 v141, 1, v141
	v_and_b32_e32 v1, 15, v1
	v_lshlrev_b32_e32 v150, 4, v141
	s_add_i32 s5, s2, s53
	v_add3_u32 v150, s5, v1, v150
	v_ashrrev_i32_e32 v151, 31, v150
	v_lshlrev_b32_e32 v141, 3, v141
	v_lshlrev_b64 v[150:151], 11, v[150:151]
	v_sub_co_u32_e32 v148, vcc, 0, v141
	v_lshl_add_u64 v[150:151], s[14:15], 0, v[150:151]
	v_lshl_add_u64 v[146:147], v[150:151], 0, v[146:147]
	v_subb_co_u32_e64 v149, s[38:39], 0, 0, vcc
	v_lshl_add_u64 v[146:147], v[146:147], 0, v[148:149]
	v_mov_b32_e32 v164, 0
	v_mov_b32_e32 v165, 0
	v_readlane_b32 s73, v255, 32
	v_readlane_b32 s74, v255, 33
	v_readlane_b32 s75, v255, 34
	v_readlane_b32 s78, v255, 37
	v_readlane_b32 s79, v255, 38
	v_readlane_b32 s82, v255, 41
	v_readlane_b32 s83, v255, 42
	v_readlane_b32 s84, v255, 43
	v_readlane_b32 s85, v255, 44
	v_readlane_b32 s86, v255, 45
	v_readlane_b32 s87, v255, 46
	s_waitcnt vmcnt(0)
	v_pk_fma_f32 v[166:167], v[128:129], s[24:25], v[136:137] op_sel_hi:[1,0,1]
	v_pk_fma_f32 v[156:157], v[130:131], s[24:25], v[138:139] op_sel_hi:[1,0,1]
	v_pk_add_f32 v[154:155], v[68:69], 1.0 op_sel_hi:[1,0]
	v_min_f32_e32 v68, 0x40e00000, v166
	v_min_f32_e32 v69, 0x40e00000, v167
	v_pk_fma_f32 v[168:169], v[126:127], s[24:25], v[134:135] op_sel_hi:[1,0,1]
	v_mul_f32_e32 v1, 0xc01d265f, v68
	v_mul_f32_e32 v141, 0xc01d265f, v69
	v_pk_add_f32 v[152:153], v[70:71], 1.0 op_sel_hi:[1,0]
	v_pk_add_f32 v[150:151], v[160:161], 1.0 op_sel_hi:[1,0]
	v_min_f32_e32 v70, 0x40e00000, v156
	v_min_f32_e32 v71, 0x40e00000, v157
	v_min_f32_e32 v160, 0x40e00000, v168
	v_min_f32_e32 v161, 0x40e00000, v169
	v_exp_f32_e32 v174, v1
	v_exp_f32_e32 v175, v141
	v_mul_f32_e32 v176, 0xc01d265f, v70
	v_mul_f32_e32 v177, 0xc01d265f, v71
	v_mul_f32_e32 v180, 0xc01d265f, v160
	v_mul_f32_e32 v181, 0xc01d265f, v161
	v_exp_f32_e32 v176, v176
	v_exp_f32_e32 v177, v177
	v_exp_f32_e32 v180, v180
	v_exp_f32_e32 v181, v181
	v_pk_add_f32 v[174:175], v[174:175], 1.0 op_sel_hi:[1,0]
	v_pk_fma_f32 v[170:171], v[124:125], s[24:25], v[132:133] op_sel_hi:[1,0,1]
	v_rcp_f32_e32 v174, v174
	v_rcp_f32_e32 v175, v175
	v_min_f32_e32 v156, 0x40e00000, v170
	v_min_f32_e32 v157, 0x40e00000, v171
	v_pk_add_f32 v[176:177], v[176:177], 1.0 op_sel_hi:[1,0]
	v_pk_add_f32 v[180:181], v[180:181], 1.0 op_sel_hi:[1,0]
	v_mul_f32_e32 v178, 0xc01d265f, v156
	v_mul_f32_e32 v179, 0xc01d265f, v157
	v_rcp_f32_e32 v176, v176
	v_rcp_f32_e32 v177, v177
	v_rcp_f32_e32 v180, v180
	v_rcp_f32_e32 v181, v181
	v_pk_fma_f32 v[166:167], v[96:97], s[24:25], v[154:155] op_sel_hi:[1,0,1]
	v_exp_f32_e32 v178, v178
	v_exp_f32_e32 v179, v179
	v_pk_add_f32 v[148:149], v[162:163], 1.0 op_sel_hi:[1,0]
	v_med3_f32 v166, v166, s62, v159
	v_med3_f32 v167, v167, s62, v159
	v_pk_mul_f32 v[68:69], v[68:69], v[174:175]
	v_pk_fma_f32 v[162:163], v[98:99], s[24:25], v[152:153] op_sel_hi:[1,0,1]
	v_pk_fma_f32 v[168:169], v[94:95], s[24:25], v[148:149] op_sel_hi:[1,0,1]
	v_pk_mul_f32 v[68:69], v[166:167], v[68:69]
	v_pk_fma_f32 v[172:173], v[122:123], s[24:25], v[138:139] op_sel_hi:[1,0,1]
	v_med3_f32 v162, v162, s62, v159
	v_med3_f32 v163, v163, s62, v159
	v_med3_f32 v168, v168, s62, v159
	v_med3_f32 v169, v169, s62, v159
	v_pk_mul_f32 v[70:71], v[70:71], v[176:177]
	v_pk_mul_f32 v[160:161], v[160:161], v[180:181]
	v_cvt_pk_fp8_f32 v164, v68, v69
	v_pk_add_f32 v[178:179], v[178:179], 1.0 op_sel_hi:[1,0]
	v_pk_mul_f32 v[68:69], v[162:163], v[70:71]
	v_pk_mul_f32 v[70:71], v[168:169], v[160:161]
	v_min_f32_e32 v160, 0x40e00000, v172
	v_rcp_f32_e32 v178, v178
	v_rcp_f32_e32 v179, v179
	v_min_f32_e32 v161, 0x40e00000, v173
	v_mul_f32_e32 v141, 0xc01d265f, v160
	v_exp_f32_e32 v166, v141
	v_mul_f32_e32 v141, 0xc01d265f, v161
	v_cvt_pk_fp8_f32 v164, v68, v69 op_sel:[0,0,1]
	v_pk_fma_f32 v[68:69], v[120:121], s[24:25], v[136:137] op_sel_hi:[1,0,1]
	v_exp_f32_e32 v167, v141
	v_pk_fma_f32 v[170:171], v[92:93], s[24:25], v[150:151] op_sel_hi:[1,0,1]
	v_min_f32_e32 v68, 0x40e00000, v68
	v_med3_f32 v170, v170, s62, v159
	v_med3_f32 v171, v171, s62, v159
	v_pk_mul_f32 v[156:157], v[156:157], v[178:179]
	v_min_f32_e32 v69, 0x40e00000, v69
	v_mul_f32_e32 v1, 0xc01d265f, v68
	v_pk_mul_f32 v[156:157], v[170:171], v[156:157]
	v_exp_f32_e32 v162, v1
	v_mul_f32_e32 v1, 0xc01d265f, v69
	v_cvt_pk_fp8_f32 v165, v156, v157
	v_exp_f32_e32 v163, v1
	v_pk_add_f32 v[166:167], v[166:167], 1.0 op_sel_hi:[1,0]
	v_pk_fma_f32 v[156:157], v[88:89], s[24:25], v[154:155] op_sel_hi:[1,0,1]
	v_rcp_f32_e32 v166, v166
	v_rcp_f32_e32 v167, v167
	v_cvt_pk_fp8_f32 v165, v70, v71 op_sel:[0,0,1]
	v_pk_fma_f32 v[70:71], v[90:91], s[24:25], v[152:153] op_sel_hi:[1,0,1]
	v_pk_add_f32 v[162:163], v[162:163], 1.0 op_sel_hi:[1,0]
	v_med3_f32 v70, v70, s62, v159
	v_rcp_f32_e32 v162, v162
	v_rcp_f32_e32 v163, v163
	v_med3_f32 v71, v71, s62, v159
	v_pk_mul_f32 v[160:161], v[160:161], v[166:167]
	v_med3_f32 v156, v156, s62, v159
	v_pk_mul_f32 v[70:71], v[70:71], v[160:161]
	v_pk_fma_f32 v[160:161], v[116:117], s[24:25], v[132:133] op_sel_hi:[1,0,1]
	v_med3_f32 v157, v157, s62, v159
	v_min_f32_e32 v160, 0x40e00000, v160
	v_min_f32_e32 v161, 0x40e00000, v161
	v_mul_f32_e32 v1, 0xc01d265f, v160
	v_pk_mul_f32 v[68:69], v[68:69], v[162:163]
	v_exp_f32_e32 v168, v1
	v_mul_f32_e32 v1, 0xc01d265f, v161
	v_pk_mul_f32 v[68:69], v[156:157], v[68:69]
	v_pk_fma_f32 v[156:157], v[118:119], s[24:25], v[134:135] op_sel_hi:[1,0,1]
	v_exp_f32_e32 v169, v1
	v_min_f32_e32 v156, 0x40e00000, v156
	v_min_f32_e32 v157, 0x40e00000, v157
	v_mul_f32_e32 v1, 0xc01d265f, v156
	v_exp_f32_e32 v170, v1
	v_mul_f32_e32 v1, 0xc01d265f, v157
	v_exp_f32_e32 v171, v1
	v_pk_add_f32 v[168:169], v[168:169], 1.0 op_sel_hi:[1,0]
	v_pk_fma_f32 v[166:167], v[84:85], s[24:25], v[150:151] op_sel_hi:[1,0,1]
	v_rcp_f32_e32 v168, v168
	v_rcp_f32_e32 v169, v169
	v_pk_add_f32 v[170:171], v[170:171], 1.0 op_sel_hi:[1,0]
	v_med3_f32 v166, v166, s62, v159
	v_med3_f32 v167, v167, s62, v159
	v_rcp_f32_e32 v170, v170
	v_rcp_f32_e32 v171, v171
	v_pk_mul_f32 v[160:161], v[160:161], v[168:169]
	v_pk_fma_f32 v[162:163], v[86:87], s[24:25], v[148:149] op_sel_hi:[1,0,1]
	v_pk_mul_f32 v[160:161], v[166:167], v[160:161]
	v_mov_b32_e32 v166, 0
	v_mov_b32_e32 v167, 0
	v_cvt_pk_fp8_f32 v166, v68, v69
	v_cvt_pk_fp8_f32 v167, v160, v161
	v_med3_f32 v162, v162, s62, v159
	v_med3_f32 v163, v163, s62, v159
	v_pk_mul_f32 v[68:69], v[156:157], v[170:171]
	v_cvt_pk_fp8_f32 v166, v70, v71 op_sel:[0,0,1]
	v_pk_mul_f32 v[68:69], v[162:163], v[68:69]
	v_pk_fma_f32 v[70:71], v[112:113], s[24:25], v[136:137] op_sel_hi:[1,0,1]
	v_cvt_pk_fp8_f32 v167, v68, v69 op_sel:[0,0,1]
	v_min_f32_e32 v70, 0x40e00000, v70
	v_pk_fma_f32 v[68:69], v[114:115], s[24:25], v[138:139] op_sel_hi:[1,0,1]
	v_min_f32_e32 v71, 0x40e00000, v71
	v_mul_f32_e32 v1, 0xc01d265f, v70
	v_min_f32_e32 v68, 0x40e00000, v68
	v_exp_f32_e32 v162, v1
	v_mul_f32_e32 v1, 0xc01d265f, v71
	v_permlane16_swap_b32_e32 v164, v166
	v_permlane16_swap_b32_e32 v165, v167
	v_min_f32_e32 v69, 0x40e00000, v69
	v_mul_f32_e32 v141, 0xc01d265f, v68
	v_exp_f32_e32 v163, v1
	s_cmp_le_i32 s96, 0
	s_cbranch_scc1 .Lp6bst_0
	global_store_dwordx4 v[146:147], v[164:167], off
.Lp6bst_0:
	v_pk_fma_f32 v[160:161], v[80:81], s[24:25], v[154:155] op_sel_hi:[1,0,1]
	v_pk_fma_f32 v[156:157], v[82:83], s[24:25], v[152:153] op_sel_hi:[1,0,1]
	v_exp_f32_e32 v164, v141
	v_mul_f32_e32 v141, 0xc01d265f, v69
	v_exp_f32_e32 v165, v141
	v_pk_add_f32 v[162:163], v[162:163], 1.0 op_sel_hi:[1,0]
	v_med3_f32 v160, v160, s62, v159
	v_rcp_f32_e32 v162, v162
	v_rcp_f32_e32 v163, v163
	v_pk_add_f32 v[164:165], v[164:165], 1.0 op_sel_hi:[1,0]
	v_med3_f32 v161, v161, s62, v159
	v_rcp_f32_e32 v164, v164
	v_rcp_f32_e32 v165, v165
	v_pk_mul_f32 v[70:71], v[70:71], v[162:163]
	v_med3_f32 v156, v156, s62, v159
	v_pk_mul_f32 v[70:71], v[160:161], v[70:71]
	v_pk_fma_f32 v[160:161], v[108:109], s[24:25], v[132:133] op_sel_hi:[1,0,1]
	v_med3_f32 v157, v157, s62, v159
	v_pk_mul_f32 v[68:69], v[68:69], v[164:165]
	v_min_f32_e32 v160, 0x40e00000, v160
	v_pk_mul_f32 v[156:157], v[156:157], v[68:69]
	v_pk_fma_f32 v[68:69], v[110:111], s[24:25], v[134:135] op_sel_hi:[1,0,1]
	v_min_f32_e32 v161, 0x40e00000, v161
	v_mul_f32_e32 v1, 0xc01d265f, v160
	v_min_f32_e32 v166, 0x40e00000, v68
	v_exp_f32_e32 v68, v1
	v_mul_f32_e32 v1, 0xc01d265f, v161
	v_min_f32_e32 v167, 0x40e00000, v69
	v_exp_f32_e32 v69, v1
	v_mul_f32_e32 v1, 0xc01d265f, v166
	v_exp_f32_e32 v168, v1
	v_mul_f32_e32 v1, 0xc01d265f, v167
	v_pk_add_f32 v[68:69], v[68:69], 1.0 op_sel_hi:[1,0]
	v_exp_f32_e32 v169, v1
	v_rcp_f32_e32 v68, v68
	v_rcp_f32_e32 v69, v69
	v_pk_fma_f32 v[164:165], v[76:77], s[24:25], v[150:151] op_sel_hi:[1,0,1]
	v_pk_add_f32 v[168:169], v[168:169], 1.0 op_sel_hi:[1,0]
	v_med3_f32 v164, v164, s62, v159
	v_med3_f32 v165, v165, s62, v159
	v_pk_mul_f32 v[68:69], v[160:161], v[68:69]
	v_rcp_f32_e32 v168, v168
	v_pk_mul_f32 v[160:161], v[164:165], v[68:69]
	v_mov_b32_e32 v68, 0
	v_rcp_f32_e32 v169, v169
	v_cvt_pk_fp8_f32 v68, v70, v71
	v_mov_b32_e32 v69, 0
	v_cvt_pk_fp8_f32 v69, v160, v161
	v_pk_fma_f32 v[162:163], v[78:79], s[24:25], v[148:149] op_sel_hi:[1,0,1]
	v_pk_mul_f32 v[70:71], v[166:167], v[168:169]
	v_med3_f32 v162, v162, s62, v159
	v_med3_f32 v163, v163, s62, v159
	v_cvt_pk_fp8_f32 v68, v156, v157 op_sel:[0,0,1]
	v_pk_fma_f32 v[156:157], v[104:105], s[24:25], v[136:137] op_sel_hi:[1,0,1]
	v_pk_mul_f32 v[70:71], v[162:163], v[70:71]
	v_min_f32_e32 v156, 0x40e00000, v156
	v_cvt_pk_fp8_f32 v69, v70, v71 op_sel:[0,0,1]
	v_pk_fma_f32 v[70:71], v[106:107], s[24:25], v[138:139] op_sel_hi:[1,0,1]
	v_min_f32_e32 v157, 0x40e00000, v157
	v_mul_f32_e32 v1, 0xc01d265f, v156
	v_min_f32_e32 v70, 0x40e00000, v70
	v_exp_f32_e32 v164, v1
	v_mul_f32_e32 v1, 0xc01d265f, v157
	v_min_f32_e32 v71, 0x40e00000, v71
	v_mul_f32_e32 v141, 0xc01d265f, v70
	v_exp_f32_e32 v165, v1
	v_exp_f32_e32 v166, v141
	v_mul_f32_e32 v141, 0xc01d265f, v71
	v_exp_f32_e32 v167, v141
	v_pk_add_f32 v[164:165], v[164:165], 1.0 op_sel_hi:[1,0]
	v_pk_fma_f32 v[162:163], v[72:73], s[24:25], v[154:155] op_sel_hi:[1,0,1]
	v_rcp_f32_e32 v164, v164
	v_rcp_f32_e32 v165, v165
	v_pk_add_f32 v[166:167], v[166:167], 1.0 op_sel_hi:[1,0]
	v_med3_f32 v162, v162, s62, v159
	v_rcp_f32_e32 v166, v166
	v_rcp_f32_e32 v167, v167
	v_med3_f32 v163, v163, s62, v159
	v_pk_mul_f32 v[156:157], v[156:157], v[164:165]
	v_pk_fma_f32 v[160:161], v[74:75], s[24:25], v[152:153] op_sel_hi:[1,0,1]
	v_pk_mul_f32 v[156:157], v[162:163], v[156:157]
	v_pk_fma_f32 v[162:163], v[100:101], s[24:25], v[132:133] op_sel_hi:[1,0,1]
	v_med3_f32 v160, v160, s62, v159
	v_med3_f32 v161, v161, s62, v159
	v_pk_mul_f32 v[70:71], v[70:71], v[166:167]
	v_min_f32_e32 v162, 0x40e00000, v162
	v_pk_mul_f32 v[160:161], v[160:161], v[70:71]
	v_pk_fma_f32 v[70:71], v[102:103], s[24:25], v[134:135] op_sel_hi:[1,0,1]
	v_min_f32_e32 v163, 0x40e00000, v163
	v_mul_f32_e32 v1, 0xc01d265f, v162
	v_min_f32_e32 v168, 0x40e00000, v70
	v_exp_f32_e32 v70, v1
	v_mul_f32_e32 v1, 0xc01d265f, v163
	v_min_f32_e32 v169, 0x40e00000, v71
	v_exp_f32_e32 v71, v1
	v_mul_f32_e32 v1, 0xc01d265f, v168
	v_exp_f32_e32 v170, v1
	v_mul_f32_e32 v1, 0xc01d265f, v169
	v_exp_f32_e32 v171, v1
	v_pk_add_f32 v[70:71], v[70:71], 1.0 op_sel_hi:[1,0]
	v_pk_fma_f32 v[166:167], v[28:29], s[24:25], v[150:151] op_sel_hi:[1,0,1]
	v_rcp_f32_e32 v70, v70
	v_rcp_f32_e32 v71, v71
	v_pk_add_f32 v[170:171], v[170:171], 1.0 op_sel_hi:[1,0]
	v_med3_f32 v166, v166, s62, v159
	v_med3_f32 v167, v167, s62, v159
	v_rcp_f32_e32 v170, v170
	v_rcp_f32_e32 v171, v171
	v_pk_mul_f32 v[70:71], v[162:163], v[70:71]
	v_pk_fma_f32 v[164:165], v[30:31], s[24:25], v[148:149] op_sel_hi:[1,0,1]
	v_pk_mul_f32 v[162:163], v[166:167], v[70:71]
	v_mov_b32_e32 v70, 0
	v_mov_b32_e32 v71, 0
	v_cvt_pk_fp8_f32 v70, v156, v157
	v_cvt_pk_fp8_f32 v71, v162, v163
	v_med3_f32 v164, v164, s62, v159
	v_med3_f32 v165, v165, s62, v159
	v_pk_mul_f32 v[156:157], v[168:169], v[170:171]
	v_cvt_pk_fp8_f32 v70, v160, v161 op_sel:[0,0,1]
	v_pk_mul_f32 v[156:157], v[164:165], v[156:157]
	v_pk_fma_f32 v[160:161], v[32:33], s[24:25], v[154:155] op_sel_hi:[1,0,1]
	v_cvt_pk_fp8_f32 v71, v156, v157 op_sel:[0,0,1]
	v_add_co_u32_e32 v156, vcc, s59, v146
	v_permlane16_swap_b32_e32 v68, v70
	v_permlane16_swap_b32_e32 v69, v71
	v_addc_co_u32_e32 v157, vcc, 0, v147, vcc
	s_cmp_le_i32 s96, 32
	s_cbranch_scc1 .Lp6bst_1
	global_store_dwordx4 v[156:157], v[68:71], off
.Lp6bst_1:
	v_med3_f32 v160, v160, s62, v159
	v_med3_f32 v161, v161, s62, v159
	v_pk_fma_f32 v[70:71], v[64:65], s[24:25], v[136:137] op_sel_hi:[1,0,1]
	v_pk_fma_f32 v[68:69], v[66:67], s[24:25], v[138:139] op_sel_hi:[1,0,1]
	v_min_f32_e32 v70, 0x40e00000, v70
	v_min_f32_e32 v71, 0x40e00000, v71
	v_mul_f32_e32 v1, 0xc01d265f, v70
	v_min_f32_e32 v68, 0x40e00000, v68
	v_exp_f32_e32 v162, v1
	v_mul_f32_e32 v1, 0xc01d265f, v71
	v_min_f32_e32 v69, 0x40e00000, v69
	v_mul_f32_e32 v141, 0xc01d265f, v68
	v_exp_f32_e32 v163, v1
	v_exp_f32_e32 v164, v141
	v_mul_f32_e32 v141, 0xc01d265f, v69
	v_exp_f32_e32 v165, v141
	v_pk_add_f32 v[162:163], v[162:163], 1.0 op_sel_hi:[1,0]
	v_pk_fma_f32 v[156:157], v[34:35], s[24:25], v[152:153] op_sel_hi:[1,0,1]
	v_rcp_f32_e32 v162, v162
	v_rcp_f32_e32 v163, v163
	v_pk_add_f32 v[164:165], v[164:165], 1.0 op_sel_hi:[1,0]
	v_med3_f32 v156, v156, s62, v159
	v_rcp_f32_e32 v164, v164
	v_rcp_f32_e32 v165, v165
	v_pk_mul_f32 v[70:71], v[70:71], v[162:163]
	v_med3_f32 v157, v157, s62, v159
	v_pk_mul_f32 v[70:71], v[160:161], v[70:71]
	v_pk_fma_f32 v[160:161], v[60:61], s[24:25], v[132:133] op_sel_hi:[1,0,1]
	v_pk_mul_f32 v[68:69], v[68:69], v[164:165]
	v_min_f32_e32 v160, 0x40e00000, v160
	v_pk_mul_f32 v[156:157], v[156:157], v[68:69]
	v_pk_fma_f32 v[68:69], v[62:63], s[24:25], v[134:135] op_sel_hi:[1,0,1]
	v_min_f32_e32 v161, 0x40e00000, v161
	v_mul_f32_e32 v1, 0xc01d265f, v160
	v_min_f32_e32 v166, 0x40e00000, v68
	v_exp_f32_e32 v68, v1
	v_mul_f32_e32 v1, 0xc01d265f, v161
	v_min_f32_e32 v167, 0x40e00000, v69
	v_exp_f32_e32 v69, v1
	v_mul_f32_e32 v1, 0xc01d265f, v166
	v_exp_f32_e32 v168, v1
	v_mul_f32_e32 v1, 0xc01d265f, v167
	v_pk_add_f32 v[68:69], v[68:69], 1.0 op_sel_hi:[1,0]
	v_exp_f32_e32 v169, v1
	v_rcp_f32_e32 v68, v68
	v_rcp_f32_e32 v69, v69
	v_pk_fma_f32 v[164:165], v[232:233], s[24:25], v[150:151] op_sel_hi:[1,0,1]
	v_pk_add_f32 v[168:169], v[168:169], 1.0 op_sel_hi:[1,0]
	v_med3_f32 v164, v164, s62, v159
	v_med3_f32 v165, v165, s62, v159
	v_pk_mul_f32 v[68:69], v[160:161], v[68:69]
	v_rcp_f32_e32 v168, v168
	v_pk_mul_f32 v[160:161], v[164:165], v[68:69]
	v_mov_b32_e32 v68, 0
	v_rcp_f32_e32 v169, v169
	v_cvt_pk_fp8_f32 v68, v70, v71
	v_mov_b32_e32 v69, 0
	v_cvt_pk_fp8_f32 v69, v160, v161
	v_pk_fma_f32 v[162:163], v[234:235], s[24:25], v[148:149] op_sel_hi:[1,0,1]
	v_pk_mul_f32 v[70:71], v[166:167], v[168:169]
	v_med3_f32 v162, v162, s62, v159
	v_med3_f32 v163, v163, s62, v159
	v_cvt_pk_fp8_f32 v68, v156, v157 op_sel:[0,0,1]
	v_pk_fma_f32 v[156:157], v[56:57], s[24:25], v[136:137] op_sel_hi:[1,0,1]
	v_pk_mul_f32 v[70:71], v[162:163], v[70:71]
	v_min_f32_e32 v156, 0x40e00000, v156
	v_cvt_pk_fp8_f32 v69, v70, v71 op_sel:[0,0,1]
	v_pk_fma_f32 v[70:71], v[58:59], s[24:25], v[138:139] op_sel_hi:[1,0,1]
	v_min_f32_e32 v157, 0x40e00000, v157
	v_mul_f32_e32 v1, 0xc01d265f, v156
	v_min_f32_e32 v70, 0x40e00000, v70
	v_exp_f32_e32 v164, v1
	v_mul_f32_e32 v1, 0xc01d265f, v157
	v_min_f32_e32 v71, 0x40e00000, v71
	v_mul_f32_e32 v141, 0xc01d265f, v70
	v_exp_f32_e32 v165, v1
	v_exp_f32_e32 v166, v141
	v_mul_f32_e32 v141, 0xc01d265f, v71
	v_exp_f32_e32 v167, v141
	v_pk_add_f32 v[164:165], v[164:165], 1.0 op_sel_hi:[1,0]
	v_pk_fma_f32 v[162:163], v[24:25], s[24:25], v[154:155] op_sel_hi:[1,0,1]
	v_rcp_f32_e32 v164, v164
	v_rcp_f32_e32 v165, v165
	v_pk_add_f32 v[166:167], v[166:167], 1.0 op_sel_hi:[1,0]
	v_med3_f32 v162, v162, s62, v159
	v_rcp_f32_e32 v166, v166
	v_rcp_f32_e32 v167, v167
	v_med3_f32 v163, v163, s62, v159
	v_pk_mul_f32 v[156:157], v[156:157], v[164:165]
	v_pk_fma_f32 v[160:161], v[26:27], s[24:25], v[152:153] op_sel_hi:[1,0,1]
	v_pk_mul_f32 v[156:157], v[162:163], v[156:157]
	v_pk_fma_f32 v[162:163], v[52:53], s[24:25], v[132:133] op_sel_hi:[1,0,1]
	v_med3_f32 v160, v160, s62, v159
	v_med3_f32 v161, v161, s62, v159
	v_pk_mul_f32 v[70:71], v[70:71], v[166:167]
	v_min_f32_e32 v162, 0x40e00000, v162
	v_pk_mul_f32 v[160:161], v[160:161], v[70:71]
	v_pk_fma_f32 v[70:71], v[54:55], s[24:25], v[134:135] op_sel_hi:[1,0,1]
	v_min_f32_e32 v163, 0x40e00000, v163
	v_mul_f32_e32 v1, 0xc01d265f, v162
	v_min_f32_e32 v168, 0x40e00000, v70
	v_exp_f32_e32 v70, v1
	v_mul_f32_e32 v1, 0xc01d265f, v163
	v_min_f32_e32 v169, 0x40e00000, v71
	v_exp_f32_e32 v71, v1
	v_mul_f32_e32 v1, 0xc01d265f, v168
	v_exp_f32_e32 v170, v1
	v_mul_f32_e32 v1, 0xc01d265f, v169
	v_exp_f32_e32 v171, v1
	v_pk_add_f32 v[70:71], v[70:71], 1.0 op_sel_hi:[1,0]
	v_pk_fma_f32 v[166:167], v[20:21], s[24:25], v[150:151] op_sel_hi:[1,0,1]
	v_rcp_f32_e32 v70, v70
	v_rcp_f32_e32 v71, v71
	v_pk_add_f32 v[170:171], v[170:171], 1.0 op_sel_hi:[1,0]
	v_med3_f32 v166, v166, s62, v159
	v_med3_f32 v167, v167, s62, v159
	v_rcp_f32_e32 v170, v170
	v_rcp_f32_e32 v171, v171
	v_pk_mul_f32 v[70:71], v[162:163], v[70:71]
	v_pk_fma_f32 v[164:165], v[22:23], s[24:25], v[148:149] op_sel_hi:[1,0,1]
	v_pk_mul_f32 v[162:163], v[166:167], v[70:71]
	v_mov_b32_e32 v70, 0
	v_mov_b32_e32 v71, 0
	v_cvt_pk_fp8_f32 v70, v156, v157
	v_cvt_pk_fp8_f32 v71, v162, v163
	v_med3_f32 v164, v164, s62, v159
	v_med3_f32 v165, v165, s62, v159
	v_pk_mul_f32 v[156:157], v[168:169], v[170:171]
	v_cvt_pk_fp8_f32 v70, v160, v161 op_sel:[0,0,1]
	v_pk_mul_f32 v[156:157], v[164:165], v[156:157]
	v_pk_fma_f32 v[160:161], v[16:17], s[24:25], v[154:155] op_sel_hi:[1,0,1]
	v_cvt_pk_fp8_f32 v71, v156, v157 op_sel:[0,0,1]
	v_add_co_u32_e32 v156, vcc, s63, v146
	v_permlane16_swap_b32_e32 v68, v70
	v_permlane16_swap_b32_e32 v69, v71
	v_addc_co_u32_e32 v157, vcc, 0, v147, vcc
	s_cmp_le_i32 s96, 128
	s_cbranch_scc1 .Lp6bst_2
	global_store_dwordx4 v[156:157], v[68:71], off
.Lp6bst_2:
	v_med3_f32 v160, v160, s62, v159
	v_med3_f32 v161, v161, s62, v159
	v_pk_fma_f32 v[70:71], v[48:49], s[24:25], v[136:137] op_sel_hi:[1,0,1]
	v_pk_fma_f32 v[68:69], v[50:51], s[24:25], v[138:139] op_sel_hi:[1,0,1]
	v_min_f32_e32 v70, 0x40e00000, v70
	v_min_f32_e32 v71, 0x40e00000, v71
	v_mul_f32_e32 v1, 0xc01d265f, v70
	v_min_f32_e32 v68, 0x40e00000, v68
	v_exp_f32_e32 v162, v1
	v_mul_f32_e32 v1, 0xc01d265f, v71
	v_min_f32_e32 v69, 0x40e00000, v69
	v_mul_f32_e32 v141, 0xc01d265f, v68
	v_exp_f32_e32 v163, v1
	v_exp_f32_e32 v164, v141
	v_mul_f32_e32 v141, 0xc01d265f, v69
	v_exp_f32_e32 v165, v141
	v_pk_add_f32 v[162:163], v[162:163], 1.0 op_sel_hi:[1,0]
	v_pk_fma_f32 v[156:157], v[18:19], s[24:25], v[152:153] op_sel_hi:[1,0,1]
	v_rcp_f32_e32 v162, v162
	v_rcp_f32_e32 v163, v163
	v_pk_add_f32 v[164:165], v[164:165], 1.0 op_sel_hi:[1,0]
	v_med3_f32 v156, v156, s62, v159
	v_rcp_f32_e32 v164, v164
	v_rcp_f32_e32 v165, v165
	v_pk_mul_f32 v[70:71], v[70:71], v[162:163]
	v_med3_f32 v157, v157, s62, v159
	v_pk_mul_f32 v[70:71], v[160:161], v[70:71]
	v_pk_fma_f32 v[160:161], v[44:45], s[24:25], v[132:133] op_sel_hi:[1,0,1]
	v_pk_mul_f32 v[68:69], v[68:69], v[164:165]
	v_min_f32_e32 v160, 0x40e00000, v160
	v_pk_mul_f32 v[156:157], v[156:157], v[68:69]
	v_pk_fma_f32 v[68:69], v[46:47], s[24:25], v[134:135] op_sel_hi:[1,0,1]
	v_min_f32_e32 v161, 0x40e00000, v161
	v_mul_f32_e32 v1, 0xc01d265f, v160
	v_min_f32_e32 v166, 0x40e00000, v68
	v_exp_f32_e32 v68, v1
	v_mul_f32_e32 v1, 0xc01d265f, v161
	v_min_f32_e32 v167, 0x40e00000, v69
	v_exp_f32_e32 v69, v1
	v_mul_f32_e32 v1, 0xc01d265f, v166
	v_exp_f32_e32 v168, v1
	v_mul_f32_e32 v1, 0xc01d265f, v167
	v_exp_f32_e32 v169, v1
	v_pk_add_f32 v[68:69], v[68:69], 1.0 op_sel_hi:[1,0]
	v_pk_fma_f32 v[164:165], v[12:13], s[24:25], v[150:151] op_sel_hi:[1,0,1]
	v_rcp_f32_e32 v68, v68
	v_rcp_f32_e32 v69, v69
	v_pk_add_f32 v[168:169], v[168:169], 1.0 op_sel_hi:[1,0]
	v_med3_f32 v164, v164, s62, v159
	v_med3_f32 v165, v165, s62, v159
	v_rcp_f32_e32 v168, v168
	v_rcp_f32_e32 v169, v169
	v_pk_mul_f32 v[68:69], v[160:161], v[68:69]
	v_pk_fma_f32 v[162:163], v[14:15], s[24:25], v[148:149] op_sel_hi:[1,0,1]
	v_pk_mul_f32 v[160:161], v[164:165], v[68:69]
	v_mov_b32_e32 v69, 0
	v_cvt_pk_fp8_f32 v69, v160, v161
	v_mov_b32_e32 v68, 0
	v_med3_f32 v162, v162, s62, v159
	v_med3_f32 v163, v163, s62, v159
	v_cvt_pk_fp8_f32 v68, v70, v71
	v_pk_mul_f32 v[70:71], v[166:167], v[168:169]
	v_pk_fma_f32 v[136:137], v[40:41], s[24:25], v[136:137] op_sel_hi:[1,0,1]
	v_pk_mul_f32 v[70:71], v[162:163], v[70:71]
	v_cvt_pk_fp8_f32 v68, v156, v157 op_sel:[0,0,1]
	v_cvt_pk_fp8_f32 v69, v70, v71 op_sel:[0,0,1]
	v_pk_fma_f32 v[70:71], v[42:43], s[24:25], v[138:139] op_sel_hi:[1,0,1]
	v_min_f32_e32 v136, 0x40e00000, v136
	v_min_f32_e32 v70, 0x40e00000, v70
	v_min_f32_e32 v71, 0x40e00000, v71
	v_mul_f32_e32 v141, 0xc01d265f, v70
	v_exp_f32_e32 v156, v141
	v_mul_f32_e32 v141, 0xc01d265f, v71
	v_exp_f32_e32 v157, v141
	v_min_f32_e32 v137, 0x40e00000, v137
	v_mul_f32_e32 v1, 0xc01d265f, v136
	v_pk_fma_f32 v[138:139], v[10:11], s[24:25], v[152:153] op_sel_hi:[1,0,1]
	v_pk_fma_f32 v[152:153], v[8:9], s[24:25], v[154:155] op_sel_hi:[1,0,1]
	v_exp_f32_e32 v154, v1
	v_mul_f32_e32 v1, 0xc01d265f, v137
	v_pk_add_f32 v[156:157], v[156:157], 1.0 op_sel_hi:[1,0]
	v_exp_f32_e32 v155, v1
	v_rcp_f32_e32 v156, v156
	v_rcp_f32_e32 v157, v157
	v_pk_fma_f32 v[132:133], v[36:37], s[24:25], v[132:133] op_sel_hi:[1,0,1]
	v_pk_add_f32 v[154:155], v[154:155], 1.0 op_sel_hi:[1,0]
	v_med3_f32 v138, v138, s62, v159
	v_med3_f32 v139, v139, s62, v159
	v_pk_mul_f32 v[70:71], v[70:71], v[156:157]
	v_min_f32_e32 v132, 0x40e00000, v132
	v_rcp_f32_e32 v154, v154
	v_rcp_f32_e32 v155, v155
	v_pk_mul_f32 v[138:139], v[138:139], v[70:71]
	v_pk_fma_f32 v[70:71], v[38:39], s[24:25], v[134:135] op_sel_hi:[1,0,1]
	v_min_f32_e32 v133, 0x40e00000, v133
	v_mul_f32_e32 v1, 0xc01d265f, v132
	v_pk_fma_f32 v[134:135], v[6:7], s[24:25], v[148:149] op_sel_hi:[1,0,1]
	v_pk_fma_f32 v[148:149], v[4:5], s[24:25], v[150:151] op_sel_hi:[1,0,1]
	v_min_f32_e32 v150, 0x40e00000, v70
	v_exp_f32_e32 v70, v1
	v_mul_f32_e32 v1, 0xc01d265f, v133
	v_min_f32_e32 v151, 0x40e00000, v71
	v_exp_f32_e32 v71, v1
	v_med3_f32 v152, v152, s62, v159
	v_med3_f32 v153, v153, s62, v159
	v_pk_mul_f32 v[136:137], v[136:137], v[154:155]
	v_mul_f32_e32 v1, 0xc01d265f, v150
	v_pk_mul_f32 v[136:137], v[152:153], v[136:137]
	v_exp_f32_e32 v152, v1
	v_mul_f32_e32 v1, 0xc01d265f, v151
	v_exp_f32_e32 v153, v1
	v_pk_add_f32 v[70:71], v[70:71], 1.0 op_sel_hi:[1,0]
	v_med3_f32 v148, v148, s62, v159
	v_rcp_f32_e32 v70, v70
	v_rcp_f32_e32 v71, v71
	v_pk_add_f32 v[152:153], v[152:153], 1.0 op_sel_hi:[1,0]
	v_med3_f32 v149, v149, s62, v159
	v_rcp_f32_e32 v152, v152
	v_rcp_f32_e32 v153, v153
	v_pk_mul_f32 v[70:71], v[132:133], v[70:71]
	v_med3_f32 v134, v134, s62, v159
	v_pk_mul_f32 v[132:133], v[148:149], v[70:71]
	v_mov_b32_e32 v70, 0
	v_mov_b32_e32 v71, 0
	v_cvt_pk_fp8_f32 v70, v136, v137
	v_cvt_pk_fp8_f32 v71, v132, v133
	v_med3_f32 v135, v135, s62, v159
	v_pk_mul_f32 v[132:133], v[150:151], v[152:153]
	v_cvt_pk_fp8_f32 v70, v138, v139 op_sel:[0,0,1]
	v_pk_mul_f32 v[132:133], v[134:135], v[132:133]
	s_nop 0
	v_permlane16_swap_b32_e32 v68, v70
	v_cvt_pk_fp8_f32 v71, v132, v133 op_sel:[0,0,1]
	v_add_co_u32_e32 v132, vcc, 0x50000, v146
	s_nop 0
	v_permlane16_swap_b32_e32 v69, v71
	v_addc_co_u32_e32 v133, vcc, 0, v147, vcc
	s_andn2_b64 vcc, exec, s[36:37]
	s_cmp_le_i32 s96, 160
	s_cbranch_scc1 .Lp6bst_3
	global_store_dwordx4 v[132:133], v[68:71], off
